# DIFF and GQA loops unrolled x4 over the K/V ring: slot offsets as ds_read immediates, per-tile VALU address adds and SALU slot rotation removed; DMA addresses on the scalar unit
# speedup vs baseline: 1.0069x; 1.0069x over previous
.LBB0_953:
	v_mfma_f32_32x32x16_bf16 v[114:129], v[98:101], v[130:133], 0
	s_min_i32 s28, s26, 0x101
	s_lshl_b32 s28, s28, 13
	s_add_i32 s88, s28, 0x4000
	s_add_i32 s28, s21, 0x8000
	s_mov_b32 m0, s28
	s_add_u32 s60, s56, s88
	s_addc_u32 s61, s57, s89
	v_lshl_add_u32 v181, s27, 14, v0
	global_load_lds_dwordx4 v174, s[60:61]
	s_add_i32 m0, s28, 0x2000
	s_add_u32 s62, s58, s88
	s_addc_u32 s63, s59, s89
	global_load_lds_dwordx4 v174, s[62:63]
	ds_read_b128 v[190:193], v181 offset:12288
	v_exp_f32_e32 v194, v82
	v_exp_f32_e32 v196, v83
	v_exp_f32_e32 v198, v84
	v_exp_f32_e32 v200, v85
	v_mfma_f32_32x32x16_bf16 v[98:113], v[102:105], v[134:137], 0
	ds_read_b128 v[82:85], v181 offset:12800
	v_cvt_pk_bf16_f32 v170, v194, v196
	v_cvt_pk_bf16_f32 v171, v198, v200
	v_exp_f32_e32 v202, v86
	v_exp_f32_e32 v204, v87
	s_waitcnt lgkmcnt(0)
	v_mfma_f32_32x32x16_bf16 v[114:129], v[162:165], v[138:141], v[114:129]
	v_cvt_pk_bf16_f32 v172, v202, v204
	v_exp_f32_e32 v206, v88
	v_exp_f32_e32 v208, v89
	v_mfma_f32_32x32x16_bf16 v[98:113], v[166:169], v[142:145], v[98:113]
	v_exp_f32_e32 v168, v92
	v_exp_f32_e32 v166, v93
	v_cvt_pk_bf16_f32 v173, v206, v208
	v_exp_f32_e32 v214, v90
	v_exp_f32_e32 v216, v91
	v_mfma_f32_32x32x16_bf16 v[34:49], v[190:193], v[150:153], v[34:49]
	ds_read_b128 v[86:89], v181 offset:14336
	v_cvt_pk_bf16_f32 v162, v214, v216
	v_cvt_pk_bf16_f32 v163, v168, v166
	v_exp_f32_e32 v182, v94
	v_exp_f32_e32 v180, v95
	v_mfma_f32_32x32x16_bf16 v[50:65], v[82:85], v[150:153], v[50:65]
	ds_read_b128 v[90:93], v181 offset:14848
	v_cvt_pk_bf16_f32 v164, v182, v180
	v_exp_f32_e32 v186, v96
	v_exp_f32_e32 v184, v97
	v_mfma_f32_32x32x16_bf16 v[2:17], v[190:193], v[158:161], v[2:17]
	v_cvt_pk_bf16_f32 v165, v186, v184
	v_exp_f32_e32 v195, v66
	v_exp_f32_e32 v197, v67
	v_exp_f32_e32 v199, v68
	v_exp_f32_e32 v201, v69
	v_mfma_f32_32x32x16_bf16 v[18:33], v[82:85], v[158:161], v[18:33]
	v_cvt_pk_bf16_f32 v158, v195, v197
	v_cvt_pk_bf16_f32 v159, v199, v201
	v_exp_f32_e32 v203, v70
	v_exp_f32_e32 v205, v71
	s_waitcnt lgkmcnt(0)
	v_mfma_f32_32x32x16_bf16 v[34:49], v[86:89], v[154:157], v[34:49]
	ds_read_b128 v[66:69], v188 offset:16384
	v_cvt_pk_bf16_f32 v160, v203, v205
	v_exp_f32_e32 v207, v72
	v_exp_f32_e32 v209, v73
	v_mfma_f32_32x32x16_bf16 v[50:65], v[90:93], v[154:157], v[50:65]
	ds_read_b128 v[70:73], v188 offset:20480
	v_exp_f32_e32 v169, v76
	v_exp_f32_e32 v167, v77
	v_cvt_pk_bf16_f32 v161, v207, v209
	v_exp_f32_e32 v215, v74
	v_exp_f32_e32 v217, v75
	v_pk_add_f32 v[74:75], v[178:179], v[194:195]
	v_mfma_f32_32x32x16_bf16 v[2:17], v[86:89], v[146:149], v[2:17]
	v_add_f32_e64 v74, v196, v74
	v_add_f32_e64 v75, v197, v75
	ds_read_b128 v[152:155], v188 offset:18432
	v_add_f32_e64 v74, v198, v74
	v_add_f32_e64 v75, v199, v75
	v_cvt_pk_bf16_f32 v190, v215, v217
	v_pk_add_f32 v[234:235], v[200:201], v[234:235]
	v_cvt_pk_bf16_f32 v191, v169, v167
	v_pk_add_f32 v[74:75], v[202:203], v[74:75]
	v_exp_f32_e32 v183, v78
	v_pk_add_f32 v[234:235], v[204:205], v[234:235]
	v_exp_f32_e32 v181, v79
	v_pk_add_f32 v[74:75], v[206:207], v[74:75]
	v_pk_add_f32 v[234:235], v[208:209], v[234:235]
	v_pk_add_f32 v[74:75], v[214:215], v[74:75]
	s_nop 0
	v_pk_add_f32 v[178:179], v[216:217], v[74:75]
	v_mfma_f32_32x32x16_bf16 v[18:33], v[90:93], v[146:149], v[18:33]
	v_exp_f32_e32 v187, v80
	v_exp_f32_e32 v185, v81
	ds_read_b128 v[194:197], v188 offset:22528
	v_cvt_pk_bf16_f32 v192, v183, v181
	v_cvt_pk_bf16_f32 v193, v187, v185
	s_waitcnt lgkmcnt(0)
	v_mfma_f32_32x32x16_bf16 v[82:97], v[66:69], v[130:133], 0
	ds_read_b128 v[146:149], v0 offset:8192
	v_exp_f32_e32 v198, v114
	v_exp_f32_e32 v200, v115
	v_exp_f32_e32 v202, v116
	v_exp_f32_e32 v204, v117
	v_mfma_f32_32x32x16_bf16 v[66:81], v[70:73], v[134:137], 0
	ds_read_b128 v[114:117], v0 offset:8704
	v_cvt_pk_bf16_f32 v150, v198, v200
	v_cvt_pk_bf16_f32 v151, v202, v204
	v_exp_f32_e32 v206, v118
	v_exp_f32_e32 v208, v119
	v_mfma_f32_32x32x16_bf16 v[82:97], v[152:155], v[138:141], v[82:97]
	v_cvt_pk_bf16_f32 v152, v206, v208
	v_exp_f32_e32 v214, v120
	v_exp_f32_e32 v216, v121
	v_mfma_f32_32x32x16_bf16 v[66:81], v[194:197], v[142:145], v[66:81]
	v_cvt_pk_bf16_f32 v153, v214, v216
	v_exp_f32_e32 v194, v122
	v_exp_f32_e32 v196, v123
	v_exp_f32_e32 v218, v124
	v_exp_f32_e32 v220, v125
	s_waitcnt lgkmcnt(0)
	v_mfma_f32_32x32x16_bf16 v[34:49], v[146:149], v[170:173], v[34:49]
	ds_read_b128 v[118:121], v0 offset:10240
	v_cvt_pk_bf16_f32 v154, v194, v196
	v_cvt_pk_bf16_f32 v155, v218, v220
	v_exp_f32_e32 v126, v126
	v_exp_f32_e32 v222, v127
	v_mfma_f32_32x32x16_bf16 v[50:65], v[114:117], v[170:173], v[50:65]
	ds_read_b128 v[122:125], v0 offset:10752
	v_cvt_pk_bf16_f32 v156, v126, v222
	v_exp_f32_e32 v128, v128
	v_exp_f32_e32 v170, v129
	v_mfma_f32_32x32x16_bf16 v[2:17], v[146:149], v[158:161], v[2:17]
	v_cvt_pk_bf16_f32 v157, v128, v170
	v_exp_f32_e32 v199, v98
	v_exp_f32_e32 v201, v99
	v_exp_f32_e32 v203, v100
	v_exp_f32_e32 v205, v101
	v_mfma_f32_32x32x16_bf16 v[18:33], v[114:117], v[158:161], v[18:33]
	v_cvt_pk_bf16_f32 v158, v199, v201
	v_cvt_pk_bf16_f32 v159, v203, v205
	v_exp_f32_e32 v207, v102
	v_exp_f32_e32 v209, v103
	v_pk_add_f32 v[102:103], v[168:169], v[178:179]
	s_waitcnt lgkmcnt(0)
	v_mfma_f32_32x32x16_bf16 v[34:49], v[118:121], v[162:165], v[34:49]
	v_add_f32_e64 v102, v166, v102
	v_add_f32_e64 v103, v167, v103
	ds_read_b128 v[98:101], v188 offset:16896
	v_add_f32_e64 v102, v182, v102
	v_add_f32_e64 v103, v183, v103
	v_cvt_pk_bf16_f32 v160, v207, v209
	v_pk_add_f32 v[234:235], v[180:181], v[234:235]
	v_exp_f32_e32 v215, v104
	v_pk_add_f32 v[102:103], v[186:187], v[102:103]
	v_exp_f32_e32 v217, v105
	v_pk_add_f32 v[234:235], v[184:185], v[234:235]
	v_pk_add_f32 v[102:103], v[102:103], v[198:199]
	v_pk_add_f32 v[234:235], v[200:201], v[234:235]
	v_pk_add_f32 v[102:103], v[202:203], v[102:103]
	v_pk_add_f32 v[234:235], v[204:205], v[234:235]
	v_pk_add_f32 v[114:115], v[206:207], v[102:103]
	v_mfma_f32_32x32x16_bf16 v[50:65], v[122:125], v[162:165], v[50:65]
	ds_read_b128 v[102:105], v188 offset:20992
	v_cvt_pk_bf16_f32 v161, v215, v217
	v_exp_f32_e32 v195, v106
	v_exp_f32_e32 v197, v107
	v_exp_f32_e32 v219, v108
	v_exp_f32_e32 v221, v109
	v_mfma_f32_32x32x16_bf16 v[2:17], v[118:121], v[190:193], v[2:17]
	ds_read_b128 v[162:165], v188 offset:18944
	v_cvt_pk_bf16_f32 v146, v195, v197
	v_cvt_pk_bf16_f32 v147, v219, v221
	v_exp_f32_e32 v127, v110
	v_exp_f32_e32 v223, v111
	v_pk_add_f32 v[106:107], v[208:209], v[114:115]
	v_mfma_f32_32x32x16_bf16 v[18:33], v[122:125], v[190:193], v[18:33]
	v_add_f32_e64 v106, v214, v106
	v_add_f32_e64 v107, v215, v107
	v_exp_f32_e32 v129, v112
	v_pk_add_f32 v[106:107], v[216:217], v[106:107]
	ds_read_b128 v[166:169], v188 offset:23040
	v_pk_add_f32 v[234:235], v[194:195], v[234:235]
	v_exp_f32_e32 v171, v113
	v_pk_add_f32 v[106:107], v[196:197], v[106:107]
	v_cvt_pk_bf16_f32 v148, v127, v223
	v_pk_add_f32 v[234:235], v[218:219], v[234:235]
	v_cvt_pk_bf16_f32 v149, v129, v171
	v_pk_add_f32 v[106:107], v[220:221], v[106:107]
	v_pk_add_f32 v[234:235], v[126:127], v[234:235]
	v_pk_add_f32 v[106:107], v[222:223], v[106:107]
	v_pk_add_f32 v[234:235], v[128:129], v[234:235]
	v_pk_add_f32 v[178:179], v[170:171], v[106:107]
	s_waitcnt vmcnt(0)
	s_add_i32 s26, s26, 1
	s_waitcnt vmcnt(0) lgkmcnt(0)
	s_barrier
	v_mfma_f32_32x32x16_bf16 v[114:129], v[98:101], v[130:133], 0
	s_min_i32 s28, s26, 0x101
	s_lshl_b32 s28, s28, 13
	s_add_i32 s88, s28, 0x4000
	s_add_i32 s28, s21, 0xc000
	s_mov_b32 m0, s28
	s_add_u32 s60, s56, s88
	s_addc_u32 s61, s57, s89
	global_load_lds_dwordx4 v174, s[60:61]
	s_add_i32 m0, s28, 0x2000
	s_add_u32 s62, s58, s88
	s_addc_u32 s63, s59, s89
	global_load_lds_dwordx4 v174, s[62:63]
	ds_read_b128 v[190:193], v0 offset:12288
	v_exp_f32_e32 v194, v82
	v_exp_f32_e32 v196, v83
	v_exp_f32_e32 v198, v84
	v_exp_f32_e32 v200, v85
	v_mfma_f32_32x32x16_bf16 v[98:113], v[102:105], v[134:137], 0
	ds_read_b128 v[82:85], v0 offset:12800
	v_cvt_pk_bf16_f32 v170, v194, v196
	v_cvt_pk_bf16_f32 v171, v198, v200
	v_exp_f32_e32 v202, v86
	v_exp_f32_e32 v204, v87
	s_waitcnt lgkmcnt(0)
	v_mfma_f32_32x32x16_bf16 v[114:129], v[162:165], v[138:141], v[114:129]
	v_cvt_pk_bf16_f32 v172, v202, v204
	v_exp_f32_e32 v206, v88
	v_exp_f32_e32 v208, v89
	v_mfma_f32_32x32x16_bf16 v[98:113], v[166:169], v[142:145], v[98:113]
	v_exp_f32_e32 v168, v92
	v_exp_f32_e32 v166, v93
	v_cvt_pk_bf16_f32 v173, v206, v208
	v_exp_f32_e32 v214, v90
	v_exp_f32_e32 v216, v91
	v_mfma_f32_32x32x16_bf16 v[34:49], v[190:193], v[150:153], v[34:49]
	ds_read_b128 v[86:89], v0 offset:14336
	v_cvt_pk_bf16_f32 v162, v214, v216
	v_cvt_pk_bf16_f32 v163, v168, v166
	v_exp_f32_e32 v182, v94
	v_exp_f32_e32 v180, v95
	v_mfma_f32_32x32x16_bf16 v[50:65], v[82:85], v[150:153], v[50:65]
	ds_read_b128 v[90:93], v0 offset:14848
	v_cvt_pk_bf16_f32 v164, v182, v180
	v_exp_f32_e32 v186, v96
	v_exp_f32_e32 v184, v97
	v_mfma_f32_32x32x16_bf16 v[2:17], v[190:193], v[158:161], v[2:17]
	v_cvt_pk_bf16_f32 v165, v186, v184
	v_exp_f32_e32 v195, v66
	v_exp_f32_e32 v197, v67
	v_exp_f32_e32 v199, v68
	v_exp_f32_e32 v201, v69
	v_mfma_f32_32x32x16_bf16 v[18:33], v[82:85], v[158:161], v[18:33]
	v_cvt_pk_bf16_f32 v158, v195, v197
	v_cvt_pk_bf16_f32 v159, v199, v201
	v_exp_f32_e32 v203, v70
	v_exp_f32_e32 v205, v71
	s_waitcnt lgkmcnt(0)
	v_mfma_f32_32x32x16_bf16 v[34:49], v[86:89], v[154:157], v[34:49]
	ds_read_b128 v[66:69], v188 offset:32768
	v_cvt_pk_bf16_f32 v160, v203, v205
	v_exp_f32_e32 v207, v72
	v_exp_f32_e32 v209, v73
	v_mfma_f32_32x32x16_bf16 v[50:65], v[90:93], v[154:157], v[50:65]
	ds_read_b128 v[70:73], v188 offset:36864
	v_exp_f32_e32 v169, v76
	v_exp_f32_e32 v167, v77
	v_cvt_pk_bf16_f32 v161, v207, v209
	v_exp_f32_e32 v215, v74
	v_exp_f32_e32 v217, v75
	v_pk_add_f32 v[74:75], v[178:179], v[194:195]
	v_mfma_f32_32x32x16_bf16 v[2:17], v[86:89], v[146:149], v[2:17]
	v_add_f32_e64 v74, v196, v74
	v_add_f32_e64 v75, v197, v75
	ds_read_b128 v[152:155], v188 offset:34816
	v_add_f32_e64 v74, v198, v74
	v_add_f32_e64 v75, v199, v75
	v_cvt_pk_bf16_f32 v190, v215, v217
	v_pk_add_f32 v[234:235], v[200:201], v[234:235]
	v_cvt_pk_bf16_f32 v191, v169, v167
	v_pk_add_f32 v[74:75], v[202:203], v[74:75]
	v_exp_f32_e32 v183, v78
	v_pk_add_f32 v[234:235], v[204:205], v[234:235]
	v_exp_f32_e32 v181, v79
	v_pk_add_f32 v[74:75], v[206:207], v[74:75]
	v_pk_add_f32 v[234:235], v[208:209], v[234:235]
	v_pk_add_f32 v[74:75], v[214:215], v[74:75]
	s_nop 0
	v_pk_add_f32 v[178:179], v[216:217], v[74:75]
	v_mfma_f32_32x32x16_bf16 v[18:33], v[90:93], v[146:149], v[18:33]
	v_exp_f32_e32 v187, v80
	v_exp_f32_e32 v185, v81
	ds_read_b128 v[194:197], v188 offset:38912
	v_cvt_pk_bf16_f32 v192, v183, v181
	v_cvt_pk_bf16_f32 v193, v187, v185
	s_waitcnt lgkmcnt(0)
	v_mfma_f32_32x32x16_bf16 v[82:97], v[66:69], v[130:133], 0
	ds_read_b128 v[146:149], v0 offset:24576
	v_exp_f32_e32 v198, v114
	v_exp_f32_e32 v200, v115
	v_exp_f32_e32 v202, v116
	v_exp_f32_e32 v204, v117
	v_mfma_f32_32x32x16_bf16 v[66:81], v[70:73], v[134:137], 0
	ds_read_b128 v[114:117], v0 offset:25088
	v_cvt_pk_bf16_f32 v150, v198, v200
	v_cvt_pk_bf16_f32 v151, v202, v204
	v_exp_f32_e32 v206, v118
	v_exp_f32_e32 v208, v119
	v_mfma_f32_32x32x16_bf16 v[82:97], v[152:155], v[138:141], v[82:97]
	v_cvt_pk_bf16_f32 v152, v206, v208
	v_exp_f32_e32 v214, v120
	v_exp_f32_e32 v216, v121
	v_mfma_f32_32x32x16_bf16 v[66:81], v[194:197], v[142:145], v[66:81]
	v_cvt_pk_bf16_f32 v153, v214, v216
	v_exp_f32_e32 v194, v122
	v_exp_f32_e32 v196, v123
	v_exp_f32_e32 v218, v124
	v_exp_f32_e32 v220, v125
	s_waitcnt lgkmcnt(0)
	v_mfma_f32_32x32x16_bf16 v[34:49], v[146:149], v[170:173], v[34:49]
	ds_read_b128 v[118:121], v0 offset:26624
	v_cvt_pk_bf16_f32 v154, v194, v196
	v_cvt_pk_bf16_f32 v155, v218, v220
	v_exp_f32_e32 v126, v126
	v_exp_f32_e32 v222, v127
	v_mfma_f32_32x32x16_bf16 v[50:65], v[114:117], v[170:173], v[50:65]
	ds_read_b128 v[122:125], v0 offset:27136
	v_cvt_pk_bf16_f32 v156, v126, v222
	v_exp_f32_e32 v128, v128
	v_exp_f32_e32 v170, v129
	v_mfma_f32_32x32x16_bf16 v[2:17], v[146:149], v[158:161], v[2:17]
	v_cvt_pk_bf16_f32 v157, v128, v170
	v_exp_f32_e32 v199, v98
	v_exp_f32_e32 v201, v99
	v_exp_f32_e32 v203, v100
	v_exp_f32_e32 v205, v101
	v_mfma_f32_32x32x16_bf16 v[18:33], v[114:117], v[158:161], v[18:33]
	v_cvt_pk_bf16_f32 v158, v199, v201
	v_cvt_pk_bf16_f32 v159, v203, v205
	v_exp_f32_e32 v207, v102
	v_exp_f32_e32 v209, v103
	v_pk_add_f32 v[102:103], v[168:169], v[178:179]
	s_waitcnt lgkmcnt(0)
	v_mfma_f32_32x32x16_bf16 v[34:49], v[118:121], v[162:165], v[34:49]
	v_add_f32_e64 v102, v166, v102
	v_add_f32_e64 v103, v167, v103
	ds_read_b128 v[98:101], v188 offset:33280
	v_add_f32_e64 v102, v182, v102
	v_add_f32_e64 v103, v183, v103
	v_cvt_pk_bf16_f32 v160, v207, v209
	v_pk_add_f32 v[234:235], v[180:181], v[234:235]
	v_exp_f32_e32 v215, v104
	v_pk_add_f32 v[102:103], v[186:187], v[102:103]
	v_exp_f32_e32 v217, v105
	v_pk_add_f32 v[234:235], v[184:185], v[234:235]
	v_pk_add_f32 v[102:103], v[102:103], v[198:199]
	v_pk_add_f32 v[234:235], v[200:201], v[234:235]
	v_pk_add_f32 v[102:103], v[202:203], v[102:103]
	v_pk_add_f32 v[234:235], v[204:205], v[234:235]
	v_pk_add_f32 v[114:115], v[206:207], v[102:103]
	v_mfma_f32_32x32x16_bf16 v[50:65], v[122:125], v[162:165], v[50:65]
	ds_read_b128 v[102:105], v188 offset:37376
	v_cvt_pk_bf16_f32 v161, v215, v217
	v_exp_f32_e32 v195, v106
	v_exp_f32_e32 v197, v107
	v_exp_f32_e32 v219, v108
	v_exp_f32_e32 v221, v109
	v_mfma_f32_32x32x16_bf16 v[2:17], v[118:121], v[190:193], v[2:17]
	ds_read_b128 v[162:165], v188 offset:35328
	v_cvt_pk_bf16_f32 v146, v195, v197
	v_cvt_pk_bf16_f32 v147, v219, v221
	v_exp_f32_e32 v127, v110
	v_exp_f32_e32 v223, v111
	v_pk_add_f32 v[106:107], v[208:209], v[114:115]
	v_mfma_f32_32x32x16_bf16 v[18:33], v[122:125], v[190:193], v[18:33]
	v_add_f32_e64 v106, v214, v106
	v_add_f32_e64 v107, v215, v107
	v_exp_f32_e32 v129, v112
	v_pk_add_f32 v[106:107], v[216:217], v[106:107]
	ds_read_b128 v[166:169], v188 offset:39424
	v_pk_add_f32 v[234:235], v[194:195], v[234:235]
	v_exp_f32_e32 v171, v113
	v_pk_add_f32 v[106:107], v[196:197], v[106:107]
	v_cvt_pk_bf16_f32 v148, v127, v223
	v_pk_add_f32 v[234:235], v[218:219], v[234:235]
	v_cvt_pk_bf16_f32 v149, v129, v171
	v_pk_add_f32 v[106:107], v[220:221], v[106:107]
	v_pk_add_f32 v[234:235], v[126:127], v[234:235]
	v_pk_add_f32 v[106:107], v[222:223], v[106:107]
	v_pk_add_f32 v[234:235], v[128:129], v[234:235]
	v_pk_add_f32 v[178:179], v[170:171], v[106:107]
	s_waitcnt vmcnt(0)
	s_add_i32 s26, s26, 1
	s_waitcnt vmcnt(0) lgkmcnt(0)
	s_barrier
	v_mfma_f32_32x32x16_bf16 v[114:129], v[98:101], v[130:133], 0
	s_min_i32 s28, s26, 0x101
	s_lshl_b32 s28, s28, 13
	s_add_i32 s88, s28, 0x4000
	s_add_i32 s28, s21, 0x0
	s_mov_b32 m0, s28
	s_add_u32 s60, s56, s88
	s_addc_u32 s61, s57, s89
	global_load_lds_dwordx4 v174, s[60:61]
	s_add_i32 m0, s28, 0x2000
	s_add_u32 s62, s58, s88
	s_addc_u32 s63, s59, s89
	global_load_lds_dwordx4 v174, s[62:63]
	ds_read_b128 v[190:193], v0 offset:28672
	v_exp_f32_e32 v194, v82
	v_exp_f32_e32 v196, v83
	v_exp_f32_e32 v198, v84
	v_exp_f32_e32 v200, v85
	v_mfma_f32_32x32x16_bf16 v[98:113], v[102:105], v[134:137], 0
	ds_read_b128 v[82:85], v0 offset:29184
	v_cvt_pk_bf16_f32 v170, v194, v196
	v_cvt_pk_bf16_f32 v171, v198, v200
	v_exp_f32_e32 v202, v86
	v_exp_f32_e32 v204, v87
	s_waitcnt lgkmcnt(0)
	v_mfma_f32_32x32x16_bf16 v[114:129], v[162:165], v[138:141], v[114:129]
	v_cvt_pk_bf16_f32 v172, v202, v204
	v_exp_f32_e32 v206, v88
	v_exp_f32_e32 v208, v89
	v_mfma_f32_32x32x16_bf16 v[98:113], v[166:169], v[142:145], v[98:113]
	v_exp_f32_e32 v168, v92
	v_exp_f32_e32 v166, v93
	v_cvt_pk_bf16_f32 v173, v206, v208
	v_exp_f32_e32 v214, v90
	v_exp_f32_e32 v216, v91
	v_mfma_f32_32x32x16_bf16 v[34:49], v[190:193], v[150:153], v[34:49]
	ds_read_b128 v[86:89], v0 offset:30720
	v_cvt_pk_bf16_f32 v162, v214, v216
	v_cvt_pk_bf16_f32 v163, v168, v166
	v_exp_f32_e32 v182, v94
	v_exp_f32_e32 v180, v95
	v_mfma_f32_32x32x16_bf16 v[50:65], v[82:85], v[150:153], v[50:65]
	ds_read_b128 v[90:93], v0 offset:31232
	v_cvt_pk_bf16_f32 v164, v182, v180
	v_exp_f32_e32 v186, v96
	v_exp_f32_e32 v184, v97
	v_mfma_f32_32x32x16_bf16 v[2:17], v[190:193], v[158:161], v[2:17]
	v_cvt_pk_bf16_f32 v165, v186, v184
	v_exp_f32_e32 v195, v66
	v_exp_f32_e32 v197, v67
	v_exp_f32_e32 v199, v68
	v_exp_f32_e32 v201, v69
	v_mfma_f32_32x32x16_bf16 v[18:33], v[82:85], v[158:161], v[18:33]
	v_cvt_pk_bf16_f32 v158, v195, v197
	v_cvt_pk_bf16_f32 v159, v199, v201
	v_exp_f32_e32 v203, v70
	v_exp_f32_e32 v205, v71
	s_waitcnt lgkmcnt(0)
	v_mfma_f32_32x32x16_bf16 v[34:49], v[86:89], v[154:157], v[34:49]
	ds_read_b128 v[66:69], v188 offset:49152
	v_cvt_pk_bf16_f32 v160, v203, v205
	v_exp_f32_e32 v207, v72
	v_exp_f32_e32 v209, v73
	v_mfma_f32_32x32x16_bf16 v[50:65], v[90:93], v[154:157], v[50:65]
	ds_read_b128 v[70:73], v188 offset:53248
	v_exp_f32_e32 v169, v76
	v_exp_f32_e32 v167, v77
	v_cvt_pk_bf16_f32 v161, v207, v209
	v_exp_f32_e32 v215, v74
	v_exp_f32_e32 v217, v75
	v_pk_add_f32 v[74:75], v[178:179], v[194:195]
	v_mfma_f32_32x32x16_bf16 v[2:17], v[86:89], v[146:149], v[2:17]
	v_add_f32_e64 v74, v196, v74
	v_add_f32_e64 v75, v197, v75
	ds_read_b128 v[152:155], v188 offset:51200
	v_add_f32_e64 v74, v198, v74
	v_add_f32_e64 v75, v199, v75
	v_cvt_pk_bf16_f32 v190, v215, v217
	v_pk_add_f32 v[234:235], v[200:201], v[234:235]
	v_cvt_pk_bf16_f32 v191, v169, v167
	v_pk_add_f32 v[74:75], v[202:203], v[74:75]
	v_exp_f32_e32 v183, v78
	v_pk_add_f32 v[234:235], v[204:205], v[234:235]
	v_exp_f32_e32 v181, v79
	v_pk_add_f32 v[74:75], v[206:207], v[74:75]
	v_pk_add_f32 v[234:235], v[208:209], v[234:235]
	v_pk_add_f32 v[74:75], v[214:215], v[74:75]
	s_nop 0
	v_pk_add_f32 v[178:179], v[216:217], v[74:75]
	v_mfma_f32_32x32x16_bf16 v[18:33], v[90:93], v[146:149], v[18:33]
	v_exp_f32_e32 v187, v80
	v_exp_f32_e32 v185, v81
	ds_read_b128 v[194:197], v188 offset:55296
	v_cvt_pk_bf16_f32 v192, v183, v181
	v_cvt_pk_bf16_f32 v193, v187, v185
	s_waitcnt lgkmcnt(0)
	v_mfma_f32_32x32x16_bf16 v[82:97], v[66:69], v[130:133], 0
	ds_read_b128 v[146:149], v0 offset:40960
	v_exp_f32_e32 v198, v114
	v_exp_f32_e32 v200, v115
	v_exp_f32_e32 v202, v116
	v_exp_f32_e32 v204, v117
	v_mfma_f32_32x32x16_bf16 v[66:81], v[70:73], v[134:137], 0
	ds_read_b128 v[114:117], v0 offset:41472
	v_cvt_pk_bf16_f32 v150, v198, v200
	v_cvt_pk_bf16_f32 v151, v202, v204
	v_exp_f32_e32 v206, v118
	v_exp_f32_e32 v208, v119
	v_mfma_f32_32x32x16_bf16 v[82:97], v[152:155], v[138:141], v[82:97]
	v_cvt_pk_bf16_f32 v152, v206, v208
	v_exp_f32_e32 v214, v120
	v_exp_f32_e32 v216, v121
	v_mfma_f32_32x32x16_bf16 v[66:81], v[194:197], v[142:145], v[66:81]
	v_cvt_pk_bf16_f32 v153, v214, v216
	v_exp_f32_e32 v194, v122
	v_exp_f32_e32 v196, v123
	v_exp_f32_e32 v218, v124
	v_exp_f32_e32 v220, v125
	s_waitcnt lgkmcnt(0)
	v_mfma_f32_32x32x16_bf16 v[34:49], v[146:149], v[170:173], v[34:49]
	ds_read_b128 v[118:121], v0 offset:43008
	v_cvt_pk_bf16_f32 v154, v194, v196
	v_cvt_pk_bf16_f32 v155, v218, v220
	v_exp_f32_e32 v126, v126
	v_exp_f32_e32 v222, v127
	v_mfma_f32_32x32x16_bf16 v[50:65], v[114:117], v[170:173], v[50:65]
	ds_read_b128 v[122:125], v0 offset:43520
	v_cvt_pk_bf16_f32 v156, v126, v222
	v_exp_f32_e32 v128, v128
	v_exp_f32_e32 v170, v129
	v_mfma_f32_32x32x16_bf16 v[2:17], v[146:149], v[158:161], v[2:17]
	v_cvt_pk_bf16_f32 v157, v128, v170
	v_exp_f32_e32 v199, v98
	v_exp_f32_e32 v201, v99
	v_exp_f32_e32 v203, v100
	v_exp_f32_e32 v205, v101
	v_mfma_f32_32x32x16_bf16 v[18:33], v[114:117], v[158:161], v[18:33]
	v_cvt_pk_bf16_f32 v158, v199, v201
	v_cvt_pk_bf16_f32 v159, v203, v205
	v_exp_f32_e32 v207, v102
	v_exp_f32_e32 v209, v103
	v_pk_add_f32 v[102:103], v[168:169], v[178:179]
	s_waitcnt lgkmcnt(0)
	v_mfma_f32_32x32x16_bf16 v[34:49], v[118:121], v[162:165], v[34:49]
	v_add_f32_e64 v102, v166, v102
	v_add_f32_e64 v103, v167, v103
	ds_read_b128 v[98:101], v188 offset:49664
	v_add_f32_e64 v102, v182, v102
	v_add_f32_e64 v103, v183, v103
	v_cvt_pk_bf16_f32 v160, v207, v209
	v_pk_add_f32 v[234:235], v[180:181], v[234:235]
	v_exp_f32_e32 v215, v104
	v_pk_add_f32 v[102:103], v[186:187], v[102:103]
	v_exp_f32_e32 v217, v105
	v_pk_add_f32 v[234:235], v[184:185], v[234:235]
	v_pk_add_f32 v[102:103], v[102:103], v[198:199]
	v_pk_add_f32 v[234:235], v[200:201], v[234:235]
	v_pk_add_f32 v[102:103], v[202:203], v[102:103]
	v_pk_add_f32 v[234:235], v[204:205], v[234:235]
	v_pk_add_f32 v[114:115], v[206:207], v[102:103]
	v_mfma_f32_32x32x16_bf16 v[50:65], v[122:125], v[162:165], v[50:65]
	ds_read_b128 v[102:105], v188 offset:53760
	v_cvt_pk_bf16_f32 v161, v215, v217
	v_exp_f32_e32 v195, v106
	v_exp_f32_e32 v197, v107
	v_exp_f32_e32 v219, v108
	v_exp_f32_e32 v221, v109
	v_mfma_f32_32x32x16_bf16 v[2:17], v[118:121], v[190:193], v[2:17]
	ds_read_b128 v[162:165], v188 offset:51712
	v_cvt_pk_bf16_f32 v146, v195, v197
	v_cvt_pk_bf16_f32 v147, v219, v221
	v_exp_f32_e32 v127, v110
	v_exp_f32_e32 v223, v111
	v_pk_add_f32 v[106:107], v[208:209], v[114:115]
	v_mfma_f32_32x32x16_bf16 v[18:33], v[122:125], v[190:193], v[18:33]
	v_add_f32_e64 v106, v214, v106
	v_add_f32_e64 v107, v215, v107
	v_exp_f32_e32 v129, v112
	v_pk_add_f32 v[106:107], v[216:217], v[106:107]
	ds_read_b128 v[166:169], v188 offset:55808
	v_pk_add_f32 v[234:235], v[194:195], v[234:235]
	v_exp_f32_e32 v171, v113
	v_pk_add_f32 v[106:107], v[196:197], v[106:107]
	v_cvt_pk_bf16_f32 v148, v127, v223
	v_pk_add_f32 v[234:235], v[218:219], v[234:235]
	v_cvt_pk_bf16_f32 v149, v129, v171
	v_pk_add_f32 v[106:107], v[220:221], v[106:107]
	v_pk_add_f32 v[234:235], v[126:127], v[234:235]
	v_pk_add_f32 v[106:107], v[222:223], v[106:107]
	v_pk_add_f32 v[234:235], v[128:129], v[234:235]
	v_pk_add_f32 v[178:179], v[170:171], v[106:107]
	s_waitcnt vmcnt(0)
	s_add_i32 s26, s26, 1
	s_waitcnt vmcnt(0) lgkmcnt(0)
	s_barrier
	v_mfma_f32_32x32x16_bf16 v[114:129], v[98:101], v[130:133], 0
	s_min_i32 s28, s26, 0x101
	s_lshl_b32 s28, s28, 13
	s_add_i32 s88, s28, 0x4000
	s_add_i32 s28, s21, 0x4000
	s_mov_b32 m0, s28
	s_add_u32 s60, s56, s88
	s_addc_u32 s61, s57, s89
	global_load_lds_dwordx4 v174, s[60:61]
	s_add_i32 m0, s28, 0x2000
	s_add_u32 s62, s58, s88
	s_addc_u32 s63, s59, s89
	global_load_lds_dwordx4 v174, s[62:63]
	ds_read_b128 v[190:193], v0 offset:45056
	v_exp_f32_e32 v194, v82
	v_exp_f32_e32 v196, v83
	v_exp_f32_e32 v198, v84
	v_exp_f32_e32 v200, v85
	v_mfma_f32_32x32x16_bf16 v[98:113], v[102:105], v[134:137], 0
	ds_read_b128 v[82:85], v0 offset:45568
	v_cvt_pk_bf16_f32 v170, v194, v196
	v_cvt_pk_bf16_f32 v171, v198, v200
	v_exp_f32_e32 v202, v86
	v_exp_f32_e32 v204, v87
	s_waitcnt lgkmcnt(0)
	v_mfma_f32_32x32x16_bf16 v[114:129], v[162:165], v[138:141], v[114:129]
	v_cvt_pk_bf16_f32 v172, v202, v204
	v_exp_f32_e32 v206, v88
	v_exp_f32_e32 v208, v89
	v_mfma_f32_32x32x16_bf16 v[98:113], v[166:169], v[142:145], v[98:113]
	v_exp_f32_e32 v168, v92
	v_exp_f32_e32 v166, v93
	v_cvt_pk_bf16_f32 v173, v206, v208
	v_exp_f32_e32 v214, v90
	v_exp_f32_e32 v216, v91
	v_mfma_f32_32x32x16_bf16 v[34:49], v[190:193], v[150:153], v[34:49]
	ds_read_b128 v[86:89], v0 offset:47104
	v_cvt_pk_bf16_f32 v162, v214, v216
	v_cvt_pk_bf16_f32 v163, v168, v166
	v_exp_f32_e32 v182, v94
	v_exp_f32_e32 v180, v95
	v_mfma_f32_32x32x16_bf16 v[50:65], v[82:85], v[150:153], v[50:65]
	ds_read_b128 v[90:93], v0 offset:47616
	v_cvt_pk_bf16_f32 v164, v182, v180
	v_exp_f32_e32 v186, v96
	v_exp_f32_e32 v184, v97
	v_mfma_f32_32x32x16_bf16 v[2:17], v[190:193], v[158:161], v[2:17]
	v_cvt_pk_bf16_f32 v165, v186, v184
	v_exp_f32_e32 v195, v66
	v_exp_f32_e32 v197, v67
	v_exp_f32_e32 v199, v68
	v_exp_f32_e32 v201, v69
	v_mfma_f32_32x32x16_bf16 v[18:33], v[82:85], v[158:161], v[18:33]
	v_cvt_pk_bf16_f32 v158, v195, v197
	v_cvt_pk_bf16_f32 v159, v199, v201
	v_exp_f32_e32 v203, v70
	v_exp_f32_e32 v205, v71
	s_waitcnt lgkmcnt(0)
	v_mfma_f32_32x32x16_bf16 v[34:49], v[86:89], v[154:157], v[34:49]
	ds_read_b128 v[66:69], v188 offset:0
	v_cvt_pk_bf16_f32 v160, v203, v205
	v_exp_f32_e32 v207, v72
	v_exp_f32_e32 v209, v73
	v_mfma_f32_32x32x16_bf16 v[50:65], v[90:93], v[154:157], v[50:65]
	ds_read_b128 v[70:73], v188 offset:4096
	v_exp_f32_e32 v169, v76
	v_exp_f32_e32 v167, v77
	v_cvt_pk_bf16_f32 v161, v207, v209
	v_exp_f32_e32 v215, v74
	v_exp_f32_e32 v217, v75
	v_pk_add_f32 v[74:75], v[178:179], v[194:195]
	v_mfma_f32_32x32x16_bf16 v[2:17], v[86:89], v[146:149], v[2:17]
	v_add_f32_e64 v74, v196, v74
	v_add_f32_e64 v75, v197, v75
	ds_read_b128 v[152:155], v188 offset:2048
	v_add_f32_e64 v74, v198, v74
	v_add_f32_e64 v75, v199, v75
	v_cvt_pk_bf16_f32 v190, v215, v217
	v_pk_add_f32 v[234:235], v[200:201], v[234:235]
	v_cvt_pk_bf16_f32 v191, v169, v167
	v_pk_add_f32 v[74:75], v[202:203], v[74:75]
	v_exp_f32_e32 v183, v78
	v_pk_add_f32 v[234:235], v[204:205], v[234:235]
	v_exp_f32_e32 v181, v79
	v_pk_add_f32 v[74:75], v[206:207], v[74:75]
	v_pk_add_f32 v[234:235], v[208:209], v[234:235]
	v_pk_add_f32 v[74:75], v[214:215], v[74:75]
	s_nop 0
	v_pk_add_f32 v[178:179], v[216:217], v[74:75]
	v_mfma_f32_32x32x16_bf16 v[18:33], v[90:93], v[146:149], v[18:33]
	v_exp_f32_e32 v187, v80
	v_exp_f32_e32 v185, v81
	ds_read_b128 v[194:197], v188 offset:6144
	v_cvt_pk_bf16_f32 v192, v183, v181
	v_cvt_pk_bf16_f32 v193, v187, v185
	s_waitcnt lgkmcnt(0)
	v_mfma_f32_32x32x16_bf16 v[82:97], v[66:69], v[130:133], 0
	ds_read_b128 v[146:149], v0 offset:57344
	v_exp_f32_e32 v198, v114
	v_exp_f32_e32 v200, v115
	v_exp_f32_e32 v202, v116
	v_exp_f32_e32 v204, v117
	v_mfma_f32_32x32x16_bf16 v[66:81], v[70:73], v[134:137], 0
	ds_read_b128 v[114:117], v0 offset:57856
	v_cvt_pk_bf16_f32 v150, v198, v200
	v_cvt_pk_bf16_f32 v151, v202, v204
	v_exp_f32_e32 v206, v118
	v_exp_f32_e32 v208, v119
	v_mfma_f32_32x32x16_bf16 v[82:97], v[152:155], v[138:141], v[82:97]
	v_cvt_pk_bf16_f32 v152, v206, v208
	v_exp_f32_e32 v214, v120
	v_exp_f32_e32 v216, v121
	v_mfma_f32_32x32x16_bf16 v[66:81], v[194:197], v[142:145], v[66:81]
	v_cvt_pk_bf16_f32 v153, v214, v216
	v_exp_f32_e32 v194, v122
	v_exp_f32_e32 v196, v123
	v_exp_f32_e32 v218, v124
	v_exp_f32_e32 v220, v125
	s_waitcnt lgkmcnt(0)
	v_mfma_f32_32x32x16_bf16 v[34:49], v[146:149], v[170:173], v[34:49]
	ds_read_b128 v[118:121], v0 offset:59392
	v_cvt_pk_bf16_f32 v154, v194, v196
	v_cvt_pk_bf16_f32 v155, v218, v220
	v_exp_f32_e32 v126, v126
	v_exp_f32_e32 v222, v127
	v_mfma_f32_32x32x16_bf16 v[50:65], v[114:117], v[170:173], v[50:65]
	ds_read_b128 v[122:125], v0 offset:59904
	v_cvt_pk_bf16_f32 v156, v126, v222
	v_exp_f32_e32 v128, v128
	v_exp_f32_e32 v170, v129
	v_mfma_f32_32x32x16_bf16 v[2:17], v[146:149], v[158:161], v[2:17]
	v_cvt_pk_bf16_f32 v157, v128, v170
	v_exp_f32_e32 v199, v98
	v_exp_f32_e32 v201, v99
	v_exp_f32_e32 v203, v100
	v_exp_f32_e32 v205, v101
	v_mfma_f32_32x32x16_bf16 v[18:33], v[114:117], v[158:161], v[18:33]
	v_cvt_pk_bf16_f32 v158, v199, v201
	v_cvt_pk_bf16_f32 v159, v203, v205
	v_exp_f32_e32 v207, v102
	v_exp_f32_e32 v209, v103
	v_pk_add_f32 v[102:103], v[168:169], v[178:179]
	s_waitcnt lgkmcnt(0)
	v_mfma_f32_32x32x16_bf16 v[34:49], v[118:121], v[162:165], v[34:49]
	v_add_f32_e64 v102, v166, v102
	v_add_f32_e64 v103, v167, v103
	ds_read_b128 v[98:101], v188 offset:512
	v_add_f32_e64 v102, v182, v102
	v_add_f32_e64 v103, v183, v103
	v_cvt_pk_bf16_f32 v160, v207, v209
	v_pk_add_f32 v[234:235], v[180:181], v[234:235]
	v_exp_f32_e32 v215, v104
	v_pk_add_f32 v[102:103], v[186:187], v[102:103]
	v_exp_f32_e32 v217, v105
	v_pk_add_f32 v[234:235], v[184:185], v[234:235]
	v_pk_add_f32 v[102:103], v[102:103], v[198:199]
	v_pk_add_f32 v[234:235], v[200:201], v[234:235]
	v_pk_add_f32 v[102:103], v[202:203], v[102:103]
	v_pk_add_f32 v[234:235], v[204:205], v[234:235]
	v_pk_add_f32 v[114:115], v[206:207], v[102:103]
	v_mfma_f32_32x32x16_bf16 v[50:65], v[122:125], v[162:165], v[50:65]
	ds_read_b128 v[102:105], v188 offset:4608
	v_cvt_pk_bf16_f32 v161, v215, v217
	v_exp_f32_e32 v195, v106
	v_exp_f32_e32 v197, v107
	v_exp_f32_e32 v219, v108
	v_exp_f32_e32 v221, v109
	v_mfma_f32_32x32x16_bf16 v[2:17], v[118:121], v[190:193], v[2:17]
	ds_read_b128 v[162:165], v188 offset:2560
	v_cvt_pk_bf16_f32 v146, v195, v197
	v_cvt_pk_bf16_f32 v147, v219, v221
	v_exp_f32_e32 v127, v110
	v_exp_f32_e32 v223, v111
	v_pk_add_f32 v[106:107], v[208:209], v[114:115]
	v_mfma_f32_32x32x16_bf16 v[18:33], v[122:125], v[190:193], v[18:33]
	v_add_f32_e64 v106, v214, v106
	v_add_f32_e64 v107, v215, v107
	v_exp_f32_e32 v129, v112
	v_pk_add_f32 v[106:107], v[216:217], v[106:107]
	ds_read_b128 v[166:169], v188 offset:6656
	v_pk_add_f32 v[234:235], v[194:195], v[234:235]
	v_exp_f32_e32 v171, v113
	v_pk_add_f32 v[106:107], v[196:197], v[106:107]
	v_cvt_pk_bf16_f32 v148, v127, v223
	v_pk_add_f32 v[234:235], v[218:219], v[234:235]
	v_cvt_pk_bf16_f32 v149, v129, v171
	v_pk_add_f32 v[106:107], v[220:221], v[106:107]
	v_pk_add_f32 v[234:235], v[126:127], v[234:235]
	v_pk_add_f32 v[106:107], v[222:223], v[106:107]
	v_pk_add_f32 v[234:235], v[128:129], v[234:235]
	v_pk_add_f32 v[178:179], v[170:171], v[106:107]
	s_waitcnt vmcnt(0)
	s_add_i32 s26, s26, 1
	s_mov_b32 s27, 3
	s_cmpk_eq_i32 s26, 0x104
	s_waitcnt vmcnt(0) lgkmcnt(0)
	s_barrier
	s_cbranch_scc0 .LBB0_953
	v_add_u32_e32 v189, 0xc000, v0
	v_add_f32_e32 v178, v178, v234
	v_add_f32_e32 v179, v179, v235
	ds_read_b128 v[66:69], v189 offset:12288
	ds_read_b128 v[70:73], v189 offset:12800
	v_mov_b32_e32 v0, v230
	s_waitcnt lgkmcnt(1)
	v_mfma_f32_32x32x16_bf16 v[34:49], v[66:69], v[150:153], v[34:49]
	s_waitcnt lgkmcnt(0)
	v_mfma_f32_32x32x16_bf16 v[50:65], v[70:73], v[150:153], v[50:65]
	v_mfma_f32_32x32x16_bf16 v[2:17], v[66:69], v[158:161], v[2:17]
	v_mfma_f32_32x32x16_bf16 v[18:33], v[70:73], v[158:161], v[18:33]
	ds_read_b128 v[68:71], v189 offset:14336
	ds_read_b128 v[72:75], v189 offset:14848
	v_mbcnt_lo_u32_b32 v76, -1, 0
	v_mbcnt_hi_u32_b32 v76, -1, v76
	v_mbcnt_lo_u32_b32 v77, -1, 0
	v_mbcnt_hi_u32_b32 v77, -1, v77
	global_load_dwordx2 v[66:67], v1, s[6:7]
	v_lshlrev_b32_e32 v77, 2, v77
	v_xor_b32_e32 v77, 0x80, v77
	v_lshlrev_b32_e32 v76, 2, v76
	ds_bpermute_b32 v77, v77, v179
	v_xor_b32_e32 v76, 0x80, v76
	ds_bpermute_b32 v76, v76, v178
	s_waitcnt lgkmcnt(3)
	v_mfma_f32_32x32x16_bf16 v[2:17], v[68:71], v[146:149], v[2:17]
	v_readfirstlane_b32 s21, v0
	s_ashr_i32 s21, s21, 1
	s_andn2_b32 s21, s21, 31
	s_cmpk_lt_i32 s21, 0x100
	s_waitcnt lgkmcnt(2)
	v_mfma_f32_32x32x16_bf16 v[18:33], v[72:75], v[146:149], v[18:33]
	v_mfma_f32_32x32x16_bf16 v[34:49], v[68:71], v[154:157], v[34:49]
	s_waitcnt lgkmcnt(1)
	v_add_f32_e32 v70, v179, v77
	v_mbcnt_lo_u32_b32 v68, -1, 0
	v_mbcnt_hi_u32_b32 v68, -1, v68
	v_rcp_f32_e32 v70, v70
	v_lshlrev_b32_e32 v69, 2, v68
	s_waitcnt lgkmcnt(0)
	v_add_f32_e32 v68, v178, v76
	v_rcp_f32_e32 v68, v68
	s_waitcnt vmcnt(0)
	v_mul_f32_e32 v66, v66, v70
	v_mfma_f32_32x32x16_bf16 v[50:65], v[72:75], v[154:157], v[50:65]
	v_mul_f32_e64 v2, v2, v66
	v_mul_f32_e64 v3, v3, v66
	v_mul_f32_e64 v18, v18, v66
	v_mul_f32_e64 v19, v19, v66
	v_mul_f32_e64 v4, v4, v66
	v_mul_f32_e64 v5, v5, v66
	v_pk_mul_f32 v[20:21], v[20:21], v[66:67] op_sel_hi:[1,0]
	v_pk_mul_f32 v[70:71], v[24:25], v[66:67] op_sel_hi:[1,0]
	v_pk_fma_f32 v[24:25], v[34:35], v[68:69], v[2:3] op_sel_hi:[1,0,1] neg_lo:[0,0,1] neg_hi:[0,0,1]
	v_pk_mul_f32 v[72:73], v[26:27], v[66:67] op_sel_hi:[1,0]
	s_nop 1
	v_pk_fma_f32 v[2:3], v[50:51], v[68:69], v[18:19] op_sel_hi:[1,0,1] neg_lo:[0,0,1] neg_hi:[0,0,1]
	v_pk_fma_f32 v[26:27], v[36:37], v[68:69], v[4:5] op_sel_hi:[1,0,1] neg_lo:[0,0,1] neg_hi:[0,0,1]
	v_pk_fma_f32 v[4:5], v[52:53], v[68:69], v[20:21] op_sel_hi:[1,0,1] neg_lo:[0,0,1] neg_hi:[0,0,1]
	v_pk_mul_f32 v[18:19], v[2:3], v[2:3]
	v_pk_mul_f32 v[6:7], v[6:7], v[66:67] op_sel_hi:[1,0]
	v_pk_mul_f32 v[22:23], v[22:23], v[66:67] op_sel_hi:[1,0]
	v_pk_mul_f32 v[36:37], v[4:5], v[4:5]
	v_pk_fma_f32 v[18:19], v[24:25], v[24:25], v[18:19]
	v_pk_mul_f32 v[74:75], v[28:29], v[66:67] op_sel_hi:[1,0]
	v_pk_fma_f32 v[28:29], v[38:39], v[68:69], v[6:7] op_sel_hi:[1,0,1] neg_lo:[0,0,1] neg_hi:[0,0,1]
	v_pk_fma_f32 v[6:7], v[54:55], v[68:69], v[22:23] op_sel_hi:[1,0,1] neg_lo:[0,0,1] neg_hi:[0,0,1]
	v_pk_fma_f32 v[36:37], v[26:27], v[26:27], v[36:37]
	v_add_f32_e32 v18, v18, v19
	v_pk_mul_f32 v[8:9], v[8:9], v[66:67] op_sel_hi:[1,0]
	v_pk_mul_f32 v[38:39], v[6:7], v[6:7]
	v_add_f32_e32 v18, v36, v18
	v_pk_mul_f32 v[76:77], v[30:31], v[66:67] op_sel_hi:[1,0]
	v_pk_fma_f32 v[30:31], v[40:41], v[68:69], v[8:9] op_sel_hi:[1,0,1] neg_lo:[0,0,1] neg_hi:[0,0,1]
	v_pk_fma_f32 v[8:9], v[56:57], v[68:69], v[70:71] op_sel_hi:[1,0,1] neg_lo:[0,0,1] neg_hi:[0,0,1]
	v_pk_fma_f32 v[38:39], v[28:29], v[28:29], v[38:39]
	v_add_f32_e32 v18, v37, v18
	v_pk_mul_f32 v[10:11], v[10:11], v[66:67] op_sel_hi:[1,0]
	v_pk_mul_f32 v[40:41], v[8:9], v[8:9]
	v_add_f32_e32 v18, v38, v18
	v_pk_mul_f32 v[78:79], v[32:33], v[66:67] op_sel_hi:[1,0]
	v_pk_fma_f32 v[32:33], v[42:43], v[68:69], v[10:11] op_sel_hi:[1,0,1] neg_lo:[0,0,1] neg_hi:[0,0,1]
	v_pk_fma_f32 v[10:11], v[58:59], v[68:69], v[72:73] op_sel_hi:[1,0,1] neg_lo:[0,0,1] neg_hi:[0,0,1]
	v_pk_fma_f32 v[40:41], v[30:31], v[30:31], v[40:41]
	v_add_f32_e32 v18, v39, v18
	v_pk_mul_f32 v[12:13], v[12:13], v[66:67] op_sel_hi:[1,0]
	v_pk_mul_f32 v[42:43], v[10:11], v[10:11]
	v_add_f32_e32 v18, v40, v18
	v_pk_fma_f32 v[34:35], v[44:45], v[68:69], v[12:13] op_sel_hi:[1,0,1] neg_lo:[0,0,1] neg_hi:[0,0,1]
	v_pk_fma_f32 v[12:13], v[60:61], v[68:69], v[74:75] op_sel_hi:[1,0,1] neg_lo:[0,0,1] neg_hi:[0,0,1]
	v_pk_fma_f32 v[42:43], v[32:33], v[32:33], v[42:43]
	v_add_f32_e32 v18, v41, v18
	v_pk_mul_f32 v[14:15], v[14:15], v[66:67] op_sel_hi:[1,0]
	v_pk_mul_f32 v[44:45], v[12:13], v[12:13]
	v_add_f32_e32 v18, v42, v18
	v_pk_fma_f32 v[20:21], v[46:47], v[68:69], v[14:15] op_sel_hi:[1,0,1] neg_lo:[0,0,1] neg_hi:[0,0,1]
	v_pk_fma_f32 v[14:15], v[62:63], v[68:69], v[76:77] op_sel_hi:[1,0,1] neg_lo:[0,0,1] neg_hi:[0,0,1]
	v_pk_fma_f32 v[44:45], v[34:35], v[34:35], v[44:45]
	v_add_f32_e32 v18, v43, v18
	v_pk_mul_f32 v[16:17], v[16:17], v[66:67] op_sel_hi:[1,0]
	v_pk_mul_f32 v[46:47], v[14:15], v[14:15]
	v_add_f32_e32 v18, v44, v18
	v_pk_fma_f32 v[22:23], v[48:49], v[68:69], v[16:17] op_sel_hi:[1,0,1] neg_lo:[0,0,1] neg_hi:[0,0,1]
	v_pk_fma_f32 v[16:17], v[64:65], v[68:69], v[78:79] op_sel_hi:[1,0,1] neg_lo:[0,0,1] neg_hi:[0,0,1]
	v_pk_fma_f32 v[46:47], v[20:21], v[20:21], v[46:47]
	v_add_f32_e32 v18, v45, v18
	v_pk_mul_f32 v[48:49], v[16:17], v[16:17]
	v_add_f32_e32 v18, v46, v18
	v_pk_fma_f32 v[48:49], v[22:23], v[22:23], v[48:49]
	v_add_f32_e32 v18, v47, v18
	v_add_f32_e32 v18, v48, v18
	v_add_f32_e32 v36, v49, v18
	v_xor_b32_e32 v18, 0x80, v69
	ds_bpermute_b32 v37, v18, v36
	s_cbranch_scc0 .LBB0_951
	s_waitcnt lgkmcnt(0)
	v_add_f32_e32 v36, v36, v37
	v_fmamk_f32 v36, v36, 0x3c800000, v224
	v_cmp_gt_f32_e32 vcc, s31, v36
	v_mul_f32_e32 v37, 0x4b800000, v36
	v_and_or_b32 v18, v0, 31, s21
	v_cndmask_b32_e32 v36, v36, v37, vcc
	v_rsq_f32_e32 v36, v36
	v_lshrrev_b32_e32 v0, 3, v0
	v_and_b32_e32 v0, 4, v0
	v_lshlrev_b32_e32 v41, 2, v0
	v_mul_f32_e32 v37, 0x45800000, v36
	v_cndmask_b32_e32 v36, v36, v37, vcc
	v_mul_f32_e32 v40, v67, v36
	global_load_dwordx4 v[36:39], v41, s[8:9] offset:128
	s_lshl_b64 s[10:11], s[10:11], 11
	s_add_u32 s10, s2, s10
	s_addc_u32 s11, s3, s11
	s_lshl_b32 s20, s20, 1
	s_add_u32 s10, s10, s20
	v_ashrrev_i32_e32 v19, 31, v18
	s_addc_u32 s11, s11, 0
	v_lshlrev_b64 v[18:19], 11, v[18:19]
	v_lshl_add_u64 v[18:19], s[10:11], 0, v[18:19]
	v_lshlrev_b32_e32 v0, 1, v0
	v_lshl_add_u64 v[18:19], v[18:19], 0, v[0:1]
	s_waitcnt vmcnt(0)
	v_pk_mul_f32 v[36:37], v[40:41], v[36:37] op_sel_hi:[0,1]
	v_pk_mul_f32 v[2:3], v[2:3], v[36:37]
	v_pk_mul_f32 v[36:37], v[40:41], v[38:39] op_sel_hi:[0,1]
	v_pk_mul_f32 v[4:5], v[4:5], v[36:37]
	global_load_dwordx4 v[36:39], v41, s[8:9] offset:160
	v_cvt_pk_bf16_f32 v2, v2, v3
	v_cvt_pk_bf16_f32 v3, v4, v5
	s_waitcnt vmcnt(0)
	v_pk_mul_f32 v[36:37], v[40:41], v[36:37] op_sel_hi:[0,1]
	v_pk_mul_f32 v[6:7], v[6:7], v[36:37]
	v_pk_mul_f32 v[36:37], v[40:41], v[38:39] op_sel_hi:[0,1]
	v_pk_mul_f32 v[8:9], v[8:9], v[36:37]
	global_load_dwordx4 v[36:39], v41, s[8:9] offset:192
	v_cvt_pk_bf16_f32 v4, v6, v7
	v_cvt_pk_bf16_f32 v5, v8, v9
	s_waitcnt vmcnt(0)
	v_pk_mul_f32 v[36:37], v[40:41], v[36:37] op_sel_hi:[0,1]
	v_pk_mul_f32 v[10:11], v[10:11], v[36:37]
	v_pk_mul_f32 v[36:37], v[40:41], v[38:39] op_sel_hi:[0,1]
	v_pk_mul_f32 v[12:13], v[12:13], v[36:37]
	global_load_dwordx4 v[36:39], v41, s[8:9] offset:224
	s_waitcnt vmcnt(0)
	v_pk_mul_f32 v[36:37], v[40:41], v[36:37] op_sel_hi:[0,1]
	v_pk_mul_f32 v[14:15], v[14:15], v[36:37]
	v_pk_mul_f32 v[36:37], v[40:41], v[38:39] op_sel_hi:[0,1]
	v_pk_mul_f32 v[16:17], v[16:17], v[36:37]
	global_load_dwordx4 v[36:39], v41, s[8:9]
	s_waitcnt vmcnt(0)
	v_pk_mul_f32 v[36:37], v[40:41], v[36:37] op_sel_hi:[0,1]
	v_pk_mul_f32 v[24:25], v[24:25], v[36:37]
	v_pk_mul_f32 v[36:37], v[40:41], v[38:39] op_sel_hi:[0,1]
	v_pk_mul_f32 v[26:27], v[26:27], v[36:37]
	global_load_dwordx4 v[36:39], v41, s[8:9] offset:32
	v_cvt_pk_bf16_f32 v24, v24, v25
	v_cvt_pk_bf16_f32 v25, v26, v27
	s_waitcnt vmcnt(0)
	v_pk_mul_f32 v[36:37], v[40:41], v[36:37] op_sel_hi:[0,1]
	v_pk_mul_f32 v[28:29], v[28:29], v[36:37]
	v_pk_mul_f32 v[36:37], v[40:41], v[38:39] op_sel_hi:[0,1]
	v_pk_mul_f32 v[30:31], v[30:31], v[36:37]
	global_load_dwordx4 v[36:39], v41, s[8:9] offset:64
	s_waitcnt vmcnt(0)
	v_pk_mul_f32 v[36:37], v[40:41], v[36:37] op_sel_hi:[0,1]
	v_pk_mul_f32 v[32:33], v[32:33], v[36:37]
	v_pk_mul_f32 v[36:37], v[40:41], v[38:39] op_sel_hi:[0,1]
	v_pk_mul_f32 v[34:35], v[34:35], v[36:37]
	global_load_dwordx4 v[36:39], v41, s[8:9] offset:96
	s_nop 0
	global_store_dwordx2 v[18:19], v[24:25], off offset:1024
	global_store_dwordx2 v[18:19], v[2:3], off offset:1088
	v_cvt_pk_bf16_f32 v2, v28, v29
	v_cvt_pk_bf16_f32 v3, v30, v31
	global_store_dwordx2 v[18:19], v[2:3], off offset:1040
	global_store_dwordx2 v[18:19], v[4:5], off offset:1104
	v_cvt_pk_bf16_f32 v2, v32, v33
	v_cvt_pk_bf16_f32 v3, v34, v35
	v_cvt_pk_bf16_f32 v4, v10, v11
	v_cvt_pk_bf16_f32 v5, v12, v13
	global_store_dwordx2 v[18:19], v[2:3], off offset:1056
	global_store_dwordx2 v[18:19], v[4:5], off offset:1120
	v_cvt_pk_bf16_f32 v4, v14, v15
	v_cvt_pk_bf16_f32 v5, v16, v17
	s_waitcnt vmcnt(6)
	v_pk_mul_f32 v[36:37], v[40:41], v[36:37] op_sel_hi:[0,1]
	v_pk_mul_f32 v[20:21], v[20:21], v[36:37]
	v_pk_mul_f32 v[36:37], v[40:41], v[38:39] op_sel_hi:[0,1]
	v_pk_mul_f32 v[22:23], v[22:23], v[36:37]
	v_cvt_pk_bf16_f32 v2, v20, v21
	v_cvt_pk_bf16_f32 v3, v22, v23
	global_store_dwordx2 v[18:19], v[2:3], off offset:1072
	global_store_dwordx2 v[18:19], v[4:5], off offset:1136
	s_branch .LBB0_951

.LBB0_967:
	v_mfma_f32_32x32x16_bf16 v[114:129], v[98:101], v[130:133], 0
	s_min_i32 s23, s21, 0x101
	s_lshl_b32 s23, s23, 13
	s_add_i32 s88, s23, 0x4000
	s_add_i32 s23, s16, 0x8000
	s_mov_b32 m0, s23
	s_add_u32 s60, s56, s88
	s_addc_u32 s61, s57, s89
	v_lshl_add_u32 v192, s22, 14, v231
	global_load_lds_dwordx4 v194, s[60:61]
	s_add_i32 m0, s23, 0x2000
	s_add_u32 s62, s58, s88
	s_addc_u32 s63, s59, s89
	global_load_lds_dwordx4 v194, s[62:63]
	ds_read_b128 v[188:191], v214 offset:4608
	v_exp_f32_e32 v216, v82
	v_exp_f32_e32 v218, v83
	v_mfma_f32_32x32x16_bf16 v[98:113], v[98:101], v[134:137], 0
	v_cvt_pk_bf16_f32 v182, v216, v218
	v_add_f32_e32 v233, v216, v233
	v_add_f32_e32 v233, v218, v233
	v_exp_f32_e32 v220, v84
	v_exp_f32_e32 v222, v85
	v_mfma_f32_32x32x16_bf16 v[114:129], v[178:181], v[138:141], v[114:129]
	ds_read_b128 v[82:85], v214 offset:6656
	v_cvt_pk_bf16_f32 v183, v220, v222
	v_add_f32_e32 v233, v220, v233
	v_add_f32_e32 v233, v222, v233
	v_exp_f32_e32 v224, v86
	v_exp_f32_e32 v238, v87
	v_mfma_f32_32x32x16_bf16 v[98:113], v[178:181], v[142:145], v[98:113]
	v_cvt_pk_bf16_f32 v184, v224, v238
	v_add_f32_e32 v233, v224, v233
	v_add_f32_e32 v233, v238, v233
	v_exp_f32_e32 v240, v88
	v_exp_f32_e32 v242, v89
	s_waitcnt lgkmcnt(1)
	v_mfma_f32_32x32x16_bf16 v[114:129], v[188:191], v[146:149], v[114:129]
	ds_read_b128 v[86:89], v192 offset:12288
	v_cvt_pk_bf16_f32 v185, v240, v242
	v_add_f32_e32 v233, v240, v233
	v_add_f32_e32 v233, v242, v233
	v_exp_f32_e32 v244, v90
	v_exp_f32_e32 v246, v91
	v_mfma_f32_32x32x16_bf16 v[98:113], v[188:191], v[150:153], v[98:113]
	ds_read_b128 v[234:237], v192 offset:12800
	v_cvt_pk_bf16_f32 v178, v244, v246
	v_add_f32_e32 v233, v244, v233
	v_add_f32_e32 v233, v246, v233
	v_exp_f32_e32 v200, v92
	v_exp_f32_e32 v198, v93
	s_waitcnt lgkmcnt(2)
	v_mfma_f32_32x32x16_bf16 v[114:129], v[82:85], v[154:157], v[114:129]
	s_nop 0
	v_cvt_pk_bf16_f32 v179, v200, v198
	v_add_f32_e32 v233, v200, v233
	v_add_f32_e32 v233, v198, v233
	v_exp_f32_e32 v204, v94
	v_exp_f32_e32 v202, v95
	v_mfma_f32_32x32x16_bf16 v[98:113], v[82:85], v[158:161], v[98:113]
	v_cvt_pk_bf16_f32 v180, v204, v202
	v_add_f32_e32 v233, v204, v233
	v_add_f32_e32 v233, v202, v233
	v_exp_f32_e32 v208, v96
	v_exp_f32_e32 v206, v97
	s_waitcnt lgkmcnt(1)
	v_mfma_f32_32x32x16_bf16 v[2:17], v[86:89], v[162:165], v[2:17]
	ds_read_b128 v[82:85], v192 offset:14336
	v_cvt_pk_bf16_f32 v181, v208, v206
	v_add_f32_e32 v233, v208, v233
	v_add_f32_e32 v233, v206, v233
	v_exp_f32_e32 v217, v66
	v_exp_f32_e32 v219, v67
	s_waitcnt lgkmcnt(1)
	v_mfma_f32_32x32x16_bf16 v[18:33], v[234:237], v[162:165], v[18:33]
	ds_read_b128 v[90:93], v192 offset:14848
	v_cvt_pk_bf16_f32 v190, v217, v219
	v_add_f32_e32 v227, v217, v227
	v_add_f32_e32 v227, v219, v227
	v_exp_f32_e32 v221, v68
	v_exp_f32_e32 v223, v69
	v_mfma_f32_32x32x16_bf16 v[34:49], v[86:89], v[174:177], v[34:49]
	v_cvt_pk_bf16_f32 v191, v221, v223
	v_add_f32_e32 v227, v221, v227
	v_add_f32_e32 v227, v223, v227
	v_exp_f32_e32 v225, v70
	v_exp_f32_e32 v239, v71
	v_mfma_f32_32x32x16_bf16 v[50:65], v[234:237], v[174:177], v[50:65]
	v_cvt_pk_bf16_f32 v192, v225, v239
	v_add_f32_e32 v227, v225, v227
	v_add_f32_e32 v227, v239, v227
	v_exp_f32_e32 v241, v72
	v_exp_f32_e32 v243, v73
	s_waitcnt lgkmcnt(1)
	v_mfma_f32_32x32x16_bf16 v[2:17], v[82:85], v[166:169], v[2:17]
	ds_read_b128 v[66:69], v215 offset:16384
	v_cvt_pk_bf16_f32 v193, v241, v243
	v_add_f32_e32 v227, v241, v227
	v_add_f32_e32 v227, v243, v227
	v_exp_f32_e32 v245, v74
	v_exp_f32_e32 v247, v75
	s_waitcnt lgkmcnt(1)
	v_mfma_f32_32x32x16_bf16 v[18:33], v[90:93], v[166:169], v[18:33]
	v_cvt_pk_bf16_f32 v186, v245, v247
	v_add_f32_e32 v227, v245, v227
	v_add_f32_e32 v227, v247, v227
	v_exp_f32_e32 v201, v76
	v_exp_f32_e32 v199, v77
	v_mfma_f32_32x32x16_bf16 v[34:49], v[82:85], v[170:173], v[34:49]
	ds_read_b128 v[164:167], v215 offset:18432
	v_cvt_pk_bf16_f32 v187, v201, v199
	v_add_f32_e32 v227, v201, v227
	v_add_f32_e32 v227, v199, v227
	v_exp_f32_e32 v205, v78
	v_exp_f32_e32 v203, v79
	v_mfma_f32_32x32x16_bf16 v[50:65], v[90:93], v[170:173], v[50:65]
	v_exp_f32_e32 v209, v80
	v_exp_f32_e32 v207, v81
	v_cvt_pk_bf16_f32 v188, v205, v203
	v_add_f32_e32 v227, v205, v227
	v_add_f32_e32 v227, v203, v227
	v_cvt_pk_bf16_f32 v189, v209, v207
	v_add_f32_e32 v227, v209, v227
	v_add_f32_e32 v227, v207, v227
	s_waitcnt lgkmcnt(1)
	v_mfma_f32_32x32x16_bf16 v[82:97], v[66:69], v[130:133], 0
	ds_read_b128 v[168:171], v215 offset:20480
	v_exp_f32_e32 v172, v114
	v_exp_f32_e32 v216, v115
	v_mfma_f32_32x32x16_bf16 v[66:81], v[66:69], v[134:137], 0
	v_cvt_pk_bf16_f32 v162, v172, v216
	v_add_f32_e32 v233, v172, v233
	v_add_f32_e32 v233, v216, v233
	v_exp_f32_e32 v218, v116
	v_exp_f32_e32 v220, v117
	s_waitcnt lgkmcnt(1)
	v_mfma_f32_32x32x16_bf16 v[82:97], v[164:167], v[138:141], v[82:97]
	ds_read_b128 v[114:117], v215 offset:22528
	v_cvt_pk_bf16_f32 v163, v218, v220
	v_add_f32_e32 v233, v218, v233
	v_add_f32_e32 v233, v220, v233
	v_exp_f32_e32 v222, v118
	v_exp_f32_e32 v224, v119
	v_mfma_f32_32x32x16_bf16 v[66:81], v[164:167], v[142:145], v[66:81]
	v_cvt_pk_bf16_f32 v164, v222, v224
	v_add_f32_e32 v233, v222, v233
	v_add_f32_e32 v233, v224, v233
	v_exp_f32_e32 v238, v120
	v_exp_f32_e32 v240, v121
	s_waitcnt lgkmcnt(1)
	v_mfma_f32_32x32x16_bf16 v[82:97], v[168:171], v[146:149], v[82:97]
	ds_read_b128 v[118:121], v0 offset:8192
	v_cvt_pk_bf16_f32 v165, v238, v240
	v_add_f32_e32 v233, v238, v233
	v_add_f32_e32 v233, v240, v233
	v_exp_f32_e32 v242, v122
	v_exp_f32_e32 v244, v123
	v_mfma_f32_32x32x16_bf16 v[66:81], v[168:171], v[150:153], v[66:81]
	ds_read_b128 v[234:237], v0 offset:8704
	v_cvt_pk_bf16_f32 v166, v242, v244
	v_add_f32_e32 v233, v242, v233
	v_add_f32_e32 v233, v244, v233
	v_exp_f32_e32 v246, v124
	v_exp_f32_e32 v248, v125
	s_waitcnt lgkmcnt(2)
	v_mfma_f32_32x32x16_bf16 v[82:97], v[114:117], v[154:157], v[82:97]
	v_cvt_pk_bf16_f32 v167, v246, v248
	v_add_f32_e32 v233, v246, v233
	v_add_f32_e32 v233, v248, v233
	v_exp_f32_e32 v126, v126
	v_exp_f32_e32 v212, v127
	v_mfma_f32_32x32x16_bf16 v[66:81], v[114:117], v[158:161], v[66:81]
	v_cvt_pk_bf16_f32 v168, v126, v212
	v_add_f32_e32 v233, v126, v233
	v_add_f32_e32 v233, v212, v233
	v_exp_f32_e32 v128, v128
	v_exp_f32_e32 v210, v129
	s_waitcnt lgkmcnt(1)
	v_mfma_f32_32x32x16_bf16 v[2:17], v[118:121], v[182:185], v[2:17]
	ds_read_b128 v[114:117], v0 offset:10240
	v_exp_f32_e32 v173, v98
	v_cvt_pk_bf16_f32 v169, v128, v210
	v_add_f32_e32 v233, v128, v233
	v_add_f32_e32 v233, v210, v233
	v_exp_f32_e32 v217, v99
	s_waitcnt lgkmcnt(1)
	v_mfma_f32_32x32x16_bf16 v[18:33], v[234:237], v[182:185], v[18:33]
	ds_read_b128 v[122:125], v0 offset:10752
	v_cvt_pk_bf16_f32 v174, v173, v217
	v_add_f32_e32 v227, v173, v227
	v_add_f32_e32 v227, v217, v227
	v_exp_f32_e32 v219, v100
	v_exp_f32_e32 v221, v101
	v_mfma_f32_32x32x16_bf16 v[34:49], v[118:121], v[190:193], v[34:49]
	v_cvt_pk_bf16_f32 v175, v219, v221
	v_add_f32_e32 v227, v219, v227
	v_add_f32_e32 v227, v221, v227
	v_exp_f32_e32 v223, v102
	v_exp_f32_e32 v225, v103
	v_mfma_f32_32x32x16_bf16 v[50:65], v[234:237], v[190:193], v[50:65]
	v_cvt_pk_bf16_f32 v176, v223, v225
	v_add_f32_e32 v227, v223, v227
	v_add_f32_e32 v227, v225, v227
	v_exp_f32_e32 v239, v104
	v_exp_f32_e32 v241, v105
	s_waitcnt lgkmcnt(1)
	v_mfma_f32_32x32x16_bf16 v[2:17], v[114:117], v[178:181], v[2:17]
	ds_read_b128 v[98:101], v215 offset:16896
	v_cvt_pk_bf16_f32 v177, v239, v241
	v_add_f32_e32 v227, v239, v227
	v_add_f32_e32 v227, v241, v227
	v_exp_f32_e32 v243, v106
	v_exp_f32_e32 v245, v107
	s_waitcnt lgkmcnt(1)
	v_mfma_f32_32x32x16_bf16 v[18:33], v[122:125], v[178:181], v[18:33]
	v_cvt_pk_bf16_f32 v170, v243, v245
	v_add_f32_e32 v227, v243, v227
	v_add_f32_e32 v227, v245, v227
	v_exp_f32_e32 v247, v108
	v_exp_f32_e32 v249, v109
	v_mfma_f32_32x32x16_bf16 v[34:49], v[114:117], v[186:189], v[34:49]
	ds_read_b128 v[178:181], v215 offset:18944
	v_cvt_pk_bf16_f32 v171, v247, v249
	v_add_f32_e32 v227, v247, v227
	v_add_f32_e32 v227, v249, v227
	v_exp_f32_e32 v127, v110
	v_exp_f32_e32 v213, v111
	v_mfma_f32_32x32x16_bf16 v[50:65], v[122:125], v[186:189], v[50:65]
	v_exp_f32_e32 v129, v112
	v_exp_f32_e32 v211, v113
	v_cvt_pk_bf16_f32 v172, v127, v213
	v_add_f32_e32 v227, v127, v227
	v_add_f32_e32 v227, v213, v227
	v_cvt_pk_bf16_f32 v173, v129, v211
	v_add_f32_e32 v227, v129, v227
	v_add_f32_e32 v227, v211, v227
	s_waitcnt vmcnt(0)
	s_add_i32 s21, s21, 1
	s_waitcnt vmcnt(0) lgkmcnt(0)
	s_barrier
	v_mfma_f32_32x32x16_bf16 v[114:129], v[98:101], v[130:133], 0
	s_min_i32 s23, s21, 0x101
	s_lshl_b32 s23, s23, 13
	s_add_i32 s88, s23, 0x4000
	s_add_i32 s23, s16, 0xc000
	s_mov_b32 m0, s23
	s_add_u32 s60, s56, s88
	s_addc_u32 s61, s57, s89
	global_load_lds_dwordx4 v194, s[60:61]
	s_add_i32 m0, s23, 0x2000
	s_add_u32 s62, s58, s88
	s_addc_u32 s63, s59, s89
	global_load_lds_dwordx4 v194, s[62:63]
	ds_read_b128 v[188:191], v214 offset:20992
	v_exp_f32_e32 v216, v82
	v_exp_f32_e32 v218, v83
	v_mfma_f32_32x32x16_bf16 v[98:113], v[98:101], v[134:137], 0
	v_cvt_pk_bf16_f32 v182, v216, v218
	v_add_f32_e32 v233, v216, v233
	v_add_f32_e32 v233, v218, v233
	v_exp_f32_e32 v220, v84
	v_exp_f32_e32 v222, v85
	v_mfma_f32_32x32x16_bf16 v[114:129], v[178:181], v[138:141], v[114:129]
	ds_read_b128 v[82:85], v214 offset:23040
	v_cvt_pk_bf16_f32 v183, v220, v222
	v_add_f32_e32 v233, v220, v233
	v_add_f32_e32 v233, v222, v233
	v_exp_f32_e32 v224, v86
	v_exp_f32_e32 v238, v87
	v_mfma_f32_32x32x16_bf16 v[98:113], v[178:181], v[142:145], v[98:113]
	v_cvt_pk_bf16_f32 v184, v224, v238
	v_add_f32_e32 v233, v224, v233
	v_add_f32_e32 v233, v238, v233
	v_exp_f32_e32 v240, v88
	v_exp_f32_e32 v242, v89
	s_waitcnt lgkmcnt(1)
	v_mfma_f32_32x32x16_bf16 v[114:129], v[188:191], v[146:149], v[114:129]
	ds_read_b128 v[86:89], v231 offset:12288
	v_cvt_pk_bf16_f32 v185, v240, v242
	v_add_f32_e32 v233, v240, v233
	v_add_f32_e32 v233, v242, v233
	v_exp_f32_e32 v244, v90
	v_exp_f32_e32 v246, v91
	v_mfma_f32_32x32x16_bf16 v[98:113], v[188:191], v[150:153], v[98:113]
	ds_read_b128 v[234:237], v231 offset:12800
	v_cvt_pk_bf16_f32 v178, v244, v246
	v_add_f32_e32 v233, v244, v233
	v_add_f32_e32 v233, v246, v233
	v_exp_f32_e32 v200, v92
	v_exp_f32_e32 v198, v93
	s_waitcnt lgkmcnt(2)
	v_mfma_f32_32x32x16_bf16 v[114:129], v[82:85], v[154:157], v[114:129]
	s_nop 0
	v_cvt_pk_bf16_f32 v179, v200, v198
	v_add_f32_e32 v233, v200, v233
	v_add_f32_e32 v233, v198, v233
	v_exp_f32_e32 v204, v94
	v_exp_f32_e32 v202, v95
	v_mfma_f32_32x32x16_bf16 v[98:113], v[82:85], v[158:161], v[98:113]
	v_cvt_pk_bf16_f32 v180, v204, v202
	v_add_f32_e32 v233, v204, v233
	v_add_f32_e32 v233, v202, v233
	v_exp_f32_e32 v208, v96
	v_exp_f32_e32 v206, v97
	s_waitcnt lgkmcnt(1)
	v_mfma_f32_32x32x16_bf16 v[2:17], v[86:89], v[162:165], v[2:17]
	ds_read_b128 v[82:85], v231 offset:14336
	v_cvt_pk_bf16_f32 v181, v208, v206
	v_add_f32_e32 v233, v208, v233
	v_add_f32_e32 v233, v206, v233
	v_exp_f32_e32 v217, v66
	v_exp_f32_e32 v219, v67
	s_waitcnt lgkmcnt(1)
	v_mfma_f32_32x32x16_bf16 v[18:33], v[234:237], v[162:165], v[18:33]
	ds_read_b128 v[90:93], v231 offset:14848
	v_cvt_pk_bf16_f32 v190, v217, v219
	v_add_f32_e32 v227, v217, v227
	v_add_f32_e32 v227, v219, v227
	v_exp_f32_e32 v221, v68
	v_exp_f32_e32 v223, v69
	v_mfma_f32_32x32x16_bf16 v[34:49], v[86:89], v[174:177], v[34:49]
	v_cvt_pk_bf16_f32 v191, v221, v223
	v_add_f32_e32 v227, v221, v227
	v_add_f32_e32 v227, v223, v227
	v_exp_f32_e32 v225, v70
	v_exp_f32_e32 v239, v71
	v_mfma_f32_32x32x16_bf16 v[50:65], v[234:237], v[174:177], v[50:65]
	v_cvt_pk_bf16_f32 v192, v225, v239
	v_add_f32_e32 v227, v225, v227
	v_add_f32_e32 v227, v239, v227
	v_exp_f32_e32 v241, v72
	v_exp_f32_e32 v243, v73
	s_waitcnt lgkmcnt(1)
	v_mfma_f32_32x32x16_bf16 v[2:17], v[82:85], v[166:169], v[2:17]
	ds_read_b128 v[66:69], v215 offset:32768
	v_cvt_pk_bf16_f32 v193, v241, v243
	v_add_f32_e32 v227, v241, v227
	v_add_f32_e32 v227, v243, v227
	v_exp_f32_e32 v245, v74
	v_exp_f32_e32 v247, v75
	s_waitcnt lgkmcnt(1)
	v_mfma_f32_32x32x16_bf16 v[18:33], v[90:93], v[166:169], v[18:33]
	v_cvt_pk_bf16_f32 v186, v245, v247
	v_add_f32_e32 v227, v245, v227
	v_add_f32_e32 v227, v247, v227
	v_exp_f32_e32 v201, v76
	v_exp_f32_e32 v199, v77
	v_mfma_f32_32x32x16_bf16 v[34:49], v[82:85], v[170:173], v[34:49]
	ds_read_b128 v[164:167], v215 offset:34816
	v_cvt_pk_bf16_f32 v187, v201, v199
	v_add_f32_e32 v227, v201, v227
	v_add_f32_e32 v227, v199, v227
	v_exp_f32_e32 v205, v78
	v_exp_f32_e32 v203, v79
	v_mfma_f32_32x32x16_bf16 v[50:65], v[90:93], v[170:173], v[50:65]
	v_exp_f32_e32 v209, v80
	v_exp_f32_e32 v207, v81
	v_cvt_pk_bf16_f32 v188, v205, v203
	v_add_f32_e32 v227, v205, v227
	v_add_f32_e32 v227, v203, v227
	v_cvt_pk_bf16_f32 v189, v209, v207
	v_add_f32_e32 v227, v209, v227
	v_add_f32_e32 v227, v207, v227
	s_waitcnt lgkmcnt(1)
	v_mfma_f32_32x32x16_bf16 v[82:97], v[66:69], v[130:133], 0
	ds_read_b128 v[168:171], v215 offset:36864
	v_exp_f32_e32 v172, v114
	v_exp_f32_e32 v216, v115
	v_mfma_f32_32x32x16_bf16 v[66:81], v[66:69], v[134:137], 0
	v_cvt_pk_bf16_f32 v162, v172, v216
	v_add_f32_e32 v233, v172, v233
	v_add_f32_e32 v233, v216, v233
	v_exp_f32_e32 v218, v116
	v_exp_f32_e32 v220, v117
	s_waitcnt lgkmcnt(1)
	v_mfma_f32_32x32x16_bf16 v[82:97], v[164:167], v[138:141], v[82:97]
	ds_read_b128 v[114:117], v215 offset:38912
	v_cvt_pk_bf16_f32 v163, v218, v220
	v_add_f32_e32 v233, v218, v233
	v_add_f32_e32 v233, v220, v233
	v_exp_f32_e32 v222, v118
	v_exp_f32_e32 v224, v119
	v_mfma_f32_32x32x16_bf16 v[66:81], v[164:167], v[142:145], v[66:81]
	v_cvt_pk_bf16_f32 v164, v222, v224
	v_add_f32_e32 v233, v222, v233
	v_add_f32_e32 v233, v224, v233
	v_exp_f32_e32 v238, v120
	v_exp_f32_e32 v240, v121
	s_waitcnt lgkmcnt(1)
	v_mfma_f32_32x32x16_bf16 v[82:97], v[168:171], v[146:149], v[82:97]
	ds_read_b128 v[118:121], v0 offset:24576
	v_cvt_pk_bf16_f32 v165, v238, v240
	v_add_f32_e32 v233, v238, v233
	v_add_f32_e32 v233, v240, v233
	v_exp_f32_e32 v242, v122
	v_exp_f32_e32 v244, v123
	v_mfma_f32_32x32x16_bf16 v[66:81], v[168:171], v[150:153], v[66:81]
	ds_read_b128 v[234:237], v0 offset:25088
	v_cvt_pk_bf16_f32 v166, v242, v244
	v_add_f32_e32 v233, v242, v233
	v_add_f32_e32 v233, v244, v233
	v_exp_f32_e32 v246, v124
	v_exp_f32_e32 v248, v125
	s_waitcnt lgkmcnt(2)
	v_mfma_f32_32x32x16_bf16 v[82:97], v[114:117], v[154:157], v[82:97]
	v_cvt_pk_bf16_f32 v167, v246, v248
	v_add_f32_e32 v233, v246, v233
	v_add_f32_e32 v233, v248, v233
	v_exp_f32_e32 v126, v126
	v_exp_f32_e32 v212, v127
	v_mfma_f32_32x32x16_bf16 v[66:81], v[114:117], v[158:161], v[66:81]
	v_cvt_pk_bf16_f32 v168, v126, v212
	v_add_f32_e32 v233, v126, v233
	v_add_f32_e32 v233, v212, v233
	v_exp_f32_e32 v128, v128
	v_exp_f32_e32 v210, v129
	s_waitcnt lgkmcnt(1)
	v_mfma_f32_32x32x16_bf16 v[2:17], v[118:121], v[182:185], v[2:17]
	ds_read_b128 v[114:117], v0 offset:26624
	v_exp_f32_e32 v173, v98
	v_cvt_pk_bf16_f32 v169, v128, v210
	v_add_f32_e32 v233, v128, v233
	v_add_f32_e32 v233, v210, v233
	v_exp_f32_e32 v217, v99
	s_waitcnt lgkmcnt(1)
	v_mfma_f32_32x32x16_bf16 v[18:33], v[234:237], v[182:185], v[18:33]
	ds_read_b128 v[122:125], v0 offset:27136
	v_cvt_pk_bf16_f32 v174, v173, v217
	v_add_f32_e32 v227, v173, v227
	v_add_f32_e32 v227, v217, v227
	v_exp_f32_e32 v219, v100
	v_exp_f32_e32 v221, v101
	v_mfma_f32_32x32x16_bf16 v[34:49], v[118:121], v[190:193], v[34:49]
	v_cvt_pk_bf16_f32 v175, v219, v221
	v_add_f32_e32 v227, v219, v227
	v_add_f32_e32 v227, v221, v227
	v_exp_f32_e32 v223, v102
	v_exp_f32_e32 v225, v103
	v_mfma_f32_32x32x16_bf16 v[50:65], v[234:237], v[190:193], v[50:65]
	v_cvt_pk_bf16_f32 v176, v223, v225
	v_add_f32_e32 v227, v223, v227
	v_add_f32_e32 v227, v225, v227
	v_exp_f32_e32 v239, v104
	v_exp_f32_e32 v241, v105
	s_waitcnt lgkmcnt(1)
	v_mfma_f32_32x32x16_bf16 v[2:17], v[114:117], v[178:181], v[2:17]
	ds_read_b128 v[98:101], v215 offset:33280
	v_cvt_pk_bf16_f32 v177, v239, v241
	v_add_f32_e32 v227, v239, v227
	v_add_f32_e32 v227, v241, v227
	v_exp_f32_e32 v243, v106
	v_exp_f32_e32 v245, v107
	s_waitcnt lgkmcnt(1)
	v_mfma_f32_32x32x16_bf16 v[18:33], v[122:125], v[178:181], v[18:33]
	v_cvt_pk_bf16_f32 v170, v243, v245
	v_add_f32_e32 v227, v243, v227
	v_add_f32_e32 v227, v245, v227
	v_exp_f32_e32 v247, v108
	v_exp_f32_e32 v249, v109
	v_mfma_f32_32x32x16_bf16 v[34:49], v[114:117], v[186:189], v[34:49]
	ds_read_b128 v[178:181], v215 offset:35328
	v_cvt_pk_bf16_f32 v171, v247, v249
	v_add_f32_e32 v227, v247, v227
	v_add_f32_e32 v227, v249, v227
	v_exp_f32_e32 v127, v110
	v_exp_f32_e32 v213, v111
	v_mfma_f32_32x32x16_bf16 v[50:65], v[122:125], v[186:189], v[50:65]
	v_exp_f32_e32 v129, v112
	v_exp_f32_e32 v211, v113
	v_cvt_pk_bf16_f32 v172, v127, v213
	v_add_f32_e32 v227, v127, v227
	v_add_f32_e32 v227, v213, v227
	v_cvt_pk_bf16_f32 v173, v129, v211
	v_add_f32_e32 v227, v129, v227
	v_add_f32_e32 v227, v211, v227
	s_waitcnt vmcnt(0)
	s_add_i32 s21, s21, 1
	s_waitcnt vmcnt(0) lgkmcnt(0)
	s_barrier
	v_mfma_f32_32x32x16_bf16 v[114:129], v[98:101], v[130:133], 0
	s_min_i32 s23, s21, 0x101
	s_lshl_b32 s23, s23, 13
	s_add_i32 s88, s23, 0x4000
	s_add_i32 s23, s16, 0x0
	s_mov_b32 m0, s23
	s_add_u32 s60, s56, s88
	s_addc_u32 s61, s57, s89
	global_load_lds_dwordx4 v194, s[60:61]
	s_add_i32 m0, s23, 0x2000
	s_add_u32 s62, s58, s88
	s_addc_u32 s63, s59, s89
	global_load_lds_dwordx4 v194, s[62:63]
	ds_read_b128 v[188:191], v214 offset:37376
	v_exp_f32_e32 v216, v82
	v_exp_f32_e32 v218, v83
	v_mfma_f32_32x32x16_bf16 v[98:113], v[98:101], v[134:137], 0
	v_cvt_pk_bf16_f32 v182, v216, v218
	v_add_f32_e32 v233, v216, v233
	v_add_f32_e32 v233, v218, v233
	v_exp_f32_e32 v220, v84
	v_exp_f32_e32 v222, v85
	v_mfma_f32_32x32x16_bf16 v[114:129], v[178:181], v[138:141], v[114:129]
	ds_read_b128 v[82:85], v214 offset:39424
	v_cvt_pk_bf16_f32 v183, v220, v222
	v_add_f32_e32 v233, v220, v233
	v_add_f32_e32 v233, v222, v233
	v_exp_f32_e32 v224, v86
	v_exp_f32_e32 v238, v87
	v_mfma_f32_32x32x16_bf16 v[98:113], v[178:181], v[142:145], v[98:113]
	v_cvt_pk_bf16_f32 v184, v224, v238
	v_add_f32_e32 v233, v224, v233
	v_add_f32_e32 v233, v238, v233
	v_exp_f32_e32 v240, v88
	v_exp_f32_e32 v242, v89
	s_waitcnt lgkmcnt(1)
	v_mfma_f32_32x32x16_bf16 v[114:129], v[188:191], v[146:149], v[114:129]
	ds_read_b128 v[86:89], v231 offset:28672
	v_cvt_pk_bf16_f32 v185, v240, v242
	v_add_f32_e32 v233, v240, v233
	v_add_f32_e32 v233, v242, v233
	v_exp_f32_e32 v244, v90
	v_exp_f32_e32 v246, v91
	v_mfma_f32_32x32x16_bf16 v[98:113], v[188:191], v[150:153], v[98:113]
	ds_read_b128 v[234:237], v231 offset:29184
	v_cvt_pk_bf16_f32 v178, v244, v246
	v_add_f32_e32 v233, v244, v233
	v_add_f32_e32 v233, v246, v233
	v_exp_f32_e32 v200, v92
	v_exp_f32_e32 v198, v93
	s_waitcnt lgkmcnt(2)
	v_mfma_f32_32x32x16_bf16 v[114:129], v[82:85], v[154:157], v[114:129]
	s_nop 0
	v_cvt_pk_bf16_f32 v179, v200, v198
	v_add_f32_e32 v233, v200, v233
	v_add_f32_e32 v233, v198, v233
	v_exp_f32_e32 v204, v94
	v_exp_f32_e32 v202, v95
	v_mfma_f32_32x32x16_bf16 v[98:113], v[82:85], v[158:161], v[98:113]
	v_cvt_pk_bf16_f32 v180, v204, v202
	v_add_f32_e32 v233, v204, v233
	v_add_f32_e32 v233, v202, v233
	v_exp_f32_e32 v208, v96
	v_exp_f32_e32 v206, v97
	s_waitcnt lgkmcnt(1)
	v_mfma_f32_32x32x16_bf16 v[2:17], v[86:89], v[162:165], v[2:17]
	ds_read_b128 v[82:85], v231 offset:30720
	v_cvt_pk_bf16_f32 v181, v208, v206
	v_add_f32_e32 v233, v208, v233
	v_add_f32_e32 v233, v206, v233
	v_exp_f32_e32 v217, v66
	v_exp_f32_e32 v219, v67
	s_waitcnt lgkmcnt(1)
	v_mfma_f32_32x32x16_bf16 v[18:33], v[234:237], v[162:165], v[18:33]
	ds_read_b128 v[90:93], v231 offset:31232
	v_cvt_pk_bf16_f32 v190, v217, v219
	v_add_f32_e32 v227, v217, v227
	v_add_f32_e32 v227, v219, v227
	v_exp_f32_e32 v221, v68
	v_exp_f32_e32 v223, v69
	v_mfma_f32_32x32x16_bf16 v[34:49], v[86:89], v[174:177], v[34:49]
	v_cvt_pk_bf16_f32 v191, v221, v223
	v_add_f32_e32 v227, v221, v227
	v_add_f32_e32 v227, v223, v227
	v_exp_f32_e32 v225, v70
	v_exp_f32_e32 v239, v71
	v_mfma_f32_32x32x16_bf16 v[50:65], v[234:237], v[174:177], v[50:65]
	v_cvt_pk_bf16_f32 v192, v225, v239
	v_add_f32_e32 v227, v225, v227
	v_add_f32_e32 v227, v239, v227
	v_exp_f32_e32 v241, v72
	v_exp_f32_e32 v243, v73
	s_waitcnt lgkmcnt(1)
	v_mfma_f32_32x32x16_bf16 v[2:17], v[82:85], v[166:169], v[2:17]
	ds_read_b128 v[66:69], v215 offset:49152
	v_cvt_pk_bf16_f32 v193, v241, v243
	v_add_f32_e32 v227, v241, v227
	v_add_f32_e32 v227, v243, v227
	v_exp_f32_e32 v245, v74
	v_exp_f32_e32 v247, v75
	s_waitcnt lgkmcnt(1)
	v_mfma_f32_32x32x16_bf16 v[18:33], v[90:93], v[166:169], v[18:33]
	v_cvt_pk_bf16_f32 v186, v245, v247
	v_add_f32_e32 v227, v245, v227
	v_add_f32_e32 v227, v247, v227
	v_exp_f32_e32 v201, v76
	v_exp_f32_e32 v199, v77
	v_mfma_f32_32x32x16_bf16 v[34:49], v[82:85], v[170:173], v[34:49]
	ds_read_b128 v[164:167], v215 offset:51200
	v_cvt_pk_bf16_f32 v187, v201, v199
	v_add_f32_e32 v227, v201, v227
	v_add_f32_e32 v227, v199, v227
	v_exp_f32_e32 v205, v78
	v_exp_f32_e32 v203, v79
	v_mfma_f32_32x32x16_bf16 v[50:65], v[90:93], v[170:173], v[50:65]
	v_exp_f32_e32 v209, v80
	v_exp_f32_e32 v207, v81
	v_cvt_pk_bf16_f32 v188, v205, v203
	v_add_f32_e32 v227, v205, v227
	v_add_f32_e32 v227, v203, v227
	v_cvt_pk_bf16_f32 v189, v209, v207
	v_add_f32_e32 v227, v209, v227
	v_add_f32_e32 v227, v207, v227
	s_waitcnt lgkmcnt(1)
	v_mfma_f32_32x32x16_bf16 v[82:97], v[66:69], v[130:133], 0
	ds_read_b128 v[168:171], v215 offset:53248
	v_exp_f32_e32 v172, v114
	v_exp_f32_e32 v216, v115
	v_mfma_f32_32x32x16_bf16 v[66:81], v[66:69], v[134:137], 0
	v_cvt_pk_bf16_f32 v162, v172, v216
	v_add_f32_e32 v233, v172, v233
	v_add_f32_e32 v233, v216, v233
	v_exp_f32_e32 v218, v116
	v_exp_f32_e32 v220, v117
	s_waitcnt lgkmcnt(1)
	v_mfma_f32_32x32x16_bf16 v[82:97], v[164:167], v[138:141], v[82:97]
	ds_read_b128 v[114:117], v215 offset:55296
	v_cvt_pk_bf16_f32 v163, v218, v220
	v_add_f32_e32 v233, v218, v233
	v_add_f32_e32 v233, v220, v233
	v_exp_f32_e32 v222, v118
	v_exp_f32_e32 v224, v119
	v_mfma_f32_32x32x16_bf16 v[66:81], v[164:167], v[142:145], v[66:81]
	v_cvt_pk_bf16_f32 v164, v222, v224
	v_add_f32_e32 v233, v222, v233
	v_add_f32_e32 v233, v224, v233
	v_exp_f32_e32 v238, v120
	v_exp_f32_e32 v240, v121
	s_waitcnt lgkmcnt(1)
	v_mfma_f32_32x32x16_bf16 v[82:97], v[168:171], v[146:149], v[82:97]
	ds_read_b128 v[118:121], v0 offset:40960
	v_cvt_pk_bf16_f32 v165, v238, v240
	v_add_f32_e32 v233, v238, v233
	v_add_f32_e32 v233, v240, v233
	v_exp_f32_e32 v242, v122
	v_exp_f32_e32 v244, v123
	v_mfma_f32_32x32x16_bf16 v[66:81], v[168:171], v[150:153], v[66:81]
	ds_read_b128 v[234:237], v0 offset:41472
	v_cvt_pk_bf16_f32 v166, v242, v244
	v_add_f32_e32 v233, v242, v233
	v_add_f32_e32 v233, v244, v233
	v_exp_f32_e32 v246, v124
	v_exp_f32_e32 v248, v125
	s_waitcnt lgkmcnt(2)
	v_mfma_f32_32x32x16_bf16 v[82:97], v[114:117], v[154:157], v[82:97]
	v_cvt_pk_bf16_f32 v167, v246, v248
	v_add_f32_e32 v233, v246, v233
	v_add_f32_e32 v233, v248, v233
	v_exp_f32_e32 v126, v126
	v_exp_f32_e32 v212, v127
	v_mfma_f32_32x32x16_bf16 v[66:81], v[114:117], v[158:161], v[66:81]
	v_cvt_pk_bf16_f32 v168, v126, v212
	v_add_f32_e32 v233, v126, v233
	v_add_f32_e32 v233, v212, v233
	v_exp_f32_e32 v128, v128
	v_exp_f32_e32 v210, v129
	s_waitcnt lgkmcnt(1)
	v_mfma_f32_32x32x16_bf16 v[2:17], v[118:121], v[182:185], v[2:17]
	ds_read_b128 v[114:117], v0 offset:43008
	v_exp_f32_e32 v173, v98
	v_cvt_pk_bf16_f32 v169, v128, v210
	v_add_f32_e32 v233, v128, v233
	v_add_f32_e32 v233, v210, v233
	v_exp_f32_e32 v217, v99
	s_waitcnt lgkmcnt(1)
	v_mfma_f32_32x32x16_bf16 v[18:33], v[234:237], v[182:185], v[18:33]
	ds_read_b128 v[122:125], v0 offset:43520
	v_cvt_pk_bf16_f32 v174, v173, v217
	v_add_f32_e32 v227, v173, v227
	v_add_f32_e32 v227, v217, v227
	v_exp_f32_e32 v219, v100
	v_exp_f32_e32 v221, v101
	v_mfma_f32_32x32x16_bf16 v[34:49], v[118:121], v[190:193], v[34:49]
	v_cvt_pk_bf16_f32 v175, v219, v221
	v_add_f32_e32 v227, v219, v227
	v_add_f32_e32 v227, v221, v227
	v_exp_f32_e32 v223, v102
	v_exp_f32_e32 v225, v103
	v_mfma_f32_32x32x16_bf16 v[50:65], v[234:237], v[190:193], v[50:65]
	v_cvt_pk_bf16_f32 v176, v223, v225
	v_add_f32_e32 v227, v223, v227
	v_add_f32_e32 v227, v225, v227
	v_exp_f32_e32 v239, v104
	v_exp_f32_e32 v241, v105
	s_waitcnt lgkmcnt(1)
	v_mfma_f32_32x32x16_bf16 v[2:17], v[114:117], v[178:181], v[2:17]
	ds_read_b128 v[98:101], v215 offset:49664
	v_cvt_pk_bf16_f32 v177, v239, v241
	v_add_f32_e32 v227, v239, v227
	v_add_f32_e32 v227, v241, v227
	v_exp_f32_e32 v243, v106
	v_exp_f32_e32 v245, v107
	s_waitcnt lgkmcnt(1)
	v_mfma_f32_32x32x16_bf16 v[18:33], v[122:125], v[178:181], v[18:33]
	v_cvt_pk_bf16_f32 v170, v243, v245
	v_add_f32_e32 v227, v243, v227
	v_add_f32_e32 v227, v245, v227
	v_exp_f32_e32 v247, v108
	v_exp_f32_e32 v249, v109
	v_mfma_f32_32x32x16_bf16 v[34:49], v[114:117], v[186:189], v[34:49]
	ds_read_b128 v[178:181], v215 offset:51712
	v_cvt_pk_bf16_f32 v171, v247, v249
	v_add_f32_e32 v227, v247, v227
	v_add_f32_e32 v227, v249, v227
	v_exp_f32_e32 v127, v110
	v_exp_f32_e32 v213, v111
	v_mfma_f32_32x32x16_bf16 v[50:65], v[122:125], v[186:189], v[50:65]
	v_exp_f32_e32 v129, v112
	v_exp_f32_e32 v211, v113
	v_cvt_pk_bf16_f32 v172, v127, v213
	v_add_f32_e32 v227, v127, v227
	v_add_f32_e32 v227, v213, v227
	v_cvt_pk_bf16_f32 v173, v129, v211
	v_add_f32_e32 v227, v129, v227
	v_add_f32_e32 v227, v211, v227
	s_waitcnt vmcnt(0)
	s_add_i32 s21, s21, 1
	s_waitcnt vmcnt(0) lgkmcnt(0)
	s_barrier
	v_mfma_f32_32x32x16_bf16 v[114:129], v[98:101], v[130:133], 0
	s_min_i32 s23, s21, 0x101
	s_lshl_b32 s23, s23, 13
	s_add_i32 s88, s23, 0x4000
	s_add_i32 s23, s16, 0x4000
	s_mov_b32 m0, s23
	s_add_u32 s60, s56, s88
	s_addc_u32 s61, s57, s89
	global_load_lds_dwordx4 v194, s[60:61]
	s_add_i32 m0, s23, 0x2000
	s_add_u32 s62, s58, s88
	s_addc_u32 s63, s59, s89
	global_load_lds_dwordx4 v194, s[62:63]
	ds_read_b128 v[188:191], v214 offset:53760
	v_exp_f32_e32 v216, v82
	v_exp_f32_e32 v218, v83
	v_mfma_f32_32x32x16_bf16 v[98:113], v[98:101], v[134:137], 0
	v_cvt_pk_bf16_f32 v182, v216, v218
	v_add_f32_e32 v233, v216, v233
	v_add_f32_e32 v233, v218, v233
	v_exp_f32_e32 v220, v84
	v_exp_f32_e32 v222, v85
	v_mfma_f32_32x32x16_bf16 v[114:129], v[178:181], v[138:141], v[114:129]
	ds_read_b128 v[82:85], v214 offset:55808
	v_cvt_pk_bf16_f32 v183, v220, v222
	v_add_f32_e32 v233, v220, v233
	v_add_f32_e32 v233, v222, v233
	v_exp_f32_e32 v224, v86
	v_exp_f32_e32 v238, v87
	v_mfma_f32_32x32x16_bf16 v[98:113], v[178:181], v[142:145], v[98:113]
	v_cvt_pk_bf16_f32 v184, v224, v238
	v_add_f32_e32 v233, v224, v233
	v_add_f32_e32 v233, v238, v233
	v_exp_f32_e32 v240, v88
	v_exp_f32_e32 v242, v89
	s_waitcnt lgkmcnt(1)
	v_mfma_f32_32x32x16_bf16 v[114:129], v[188:191], v[146:149], v[114:129]
	ds_read_b128 v[86:89], v231 offset:45056
	v_cvt_pk_bf16_f32 v185, v240, v242
	v_add_f32_e32 v233, v240, v233
	v_add_f32_e32 v233, v242, v233
	v_exp_f32_e32 v244, v90
	v_exp_f32_e32 v246, v91
	v_mfma_f32_32x32x16_bf16 v[98:113], v[188:191], v[150:153], v[98:113]
	ds_read_b128 v[234:237], v231 offset:45568
	v_cvt_pk_bf16_f32 v178, v244, v246
	v_add_f32_e32 v233, v244, v233
	v_add_f32_e32 v233, v246, v233
	v_exp_f32_e32 v200, v92
	v_exp_f32_e32 v198, v93
	s_waitcnt lgkmcnt(2)
	v_mfma_f32_32x32x16_bf16 v[114:129], v[82:85], v[154:157], v[114:129]
	s_nop 0
	v_cvt_pk_bf16_f32 v179, v200, v198
	v_add_f32_e32 v233, v200, v233
	v_add_f32_e32 v233, v198, v233
	v_exp_f32_e32 v204, v94
	v_exp_f32_e32 v202, v95
	v_mfma_f32_32x32x16_bf16 v[98:113], v[82:85], v[158:161], v[98:113]
	v_cvt_pk_bf16_f32 v180, v204, v202
	v_add_f32_e32 v233, v204, v233
	v_add_f32_e32 v233, v202, v233
	v_exp_f32_e32 v208, v96
	v_exp_f32_e32 v206, v97
	s_waitcnt lgkmcnt(1)
	v_mfma_f32_32x32x16_bf16 v[2:17], v[86:89], v[162:165], v[2:17]
	ds_read_b128 v[82:85], v231 offset:47104
	v_cvt_pk_bf16_f32 v181, v208, v206
	v_add_f32_e32 v233, v208, v233
	v_add_f32_e32 v233, v206, v233
	v_exp_f32_e32 v217, v66
	v_exp_f32_e32 v219, v67
	s_waitcnt lgkmcnt(1)
	v_mfma_f32_32x32x16_bf16 v[18:33], v[234:237], v[162:165], v[18:33]
	ds_read_b128 v[90:93], v231 offset:47616
	v_cvt_pk_bf16_f32 v190, v217, v219
	v_add_f32_e32 v227, v217, v227
	v_add_f32_e32 v227, v219, v227
	v_exp_f32_e32 v221, v68
	v_exp_f32_e32 v223, v69
	v_mfma_f32_32x32x16_bf16 v[34:49], v[86:89], v[174:177], v[34:49]
	v_cvt_pk_bf16_f32 v191, v221, v223
	v_add_f32_e32 v227, v221, v227
	v_add_f32_e32 v227, v223, v227
	v_exp_f32_e32 v225, v70
	v_exp_f32_e32 v239, v71
	v_mfma_f32_32x32x16_bf16 v[50:65], v[234:237], v[174:177], v[50:65]
	v_cvt_pk_bf16_f32 v192, v225, v239
	v_add_f32_e32 v227, v225, v227
	v_add_f32_e32 v227, v239, v227
	v_exp_f32_e32 v241, v72
	v_exp_f32_e32 v243, v73
	s_waitcnt lgkmcnt(1)
	v_mfma_f32_32x32x16_bf16 v[2:17], v[82:85], v[166:169], v[2:17]
	ds_read_b128 v[66:69], v215 offset:0
	v_cvt_pk_bf16_f32 v193, v241, v243
	v_add_f32_e32 v227, v241, v227
	v_add_f32_e32 v227, v243, v227
	v_exp_f32_e32 v245, v74
	v_exp_f32_e32 v247, v75
	s_waitcnt lgkmcnt(1)
	v_mfma_f32_32x32x16_bf16 v[18:33], v[90:93], v[166:169], v[18:33]
	v_cvt_pk_bf16_f32 v186, v245, v247
	v_add_f32_e32 v227, v245, v227
	v_add_f32_e32 v227, v247, v227
	v_exp_f32_e32 v201, v76
	v_exp_f32_e32 v199, v77
	v_mfma_f32_32x32x16_bf16 v[34:49], v[82:85], v[170:173], v[34:49]
	ds_read_b128 v[164:167], v215 offset:2048
	v_cvt_pk_bf16_f32 v187, v201, v199
	v_add_f32_e32 v227, v201, v227
	v_add_f32_e32 v227, v199, v227
	v_exp_f32_e32 v205, v78
	v_exp_f32_e32 v203, v79
	v_mfma_f32_32x32x16_bf16 v[50:65], v[90:93], v[170:173], v[50:65]
	v_exp_f32_e32 v209, v80
	v_exp_f32_e32 v207, v81
	v_cvt_pk_bf16_f32 v188, v205, v203
	v_add_f32_e32 v227, v205, v227
	v_add_f32_e32 v227, v203, v227
	v_cvt_pk_bf16_f32 v189, v209, v207
	v_add_f32_e32 v227, v209, v227
	v_add_f32_e32 v227, v207, v227
	s_waitcnt lgkmcnt(1)
	v_mfma_f32_32x32x16_bf16 v[82:97], v[66:69], v[130:133], 0
	ds_read_b128 v[168:171], v215 offset:4096
	v_exp_f32_e32 v172, v114
	v_exp_f32_e32 v216, v115
	v_mfma_f32_32x32x16_bf16 v[66:81], v[66:69], v[134:137], 0
	v_cvt_pk_bf16_f32 v162, v172, v216
	v_add_f32_e32 v233, v172, v233
	v_add_f32_e32 v233, v216, v233
	v_exp_f32_e32 v218, v116
	v_exp_f32_e32 v220, v117
	s_waitcnt lgkmcnt(1)
	v_mfma_f32_32x32x16_bf16 v[82:97], v[164:167], v[138:141], v[82:97]
	ds_read_b128 v[114:117], v215 offset:6144
	v_cvt_pk_bf16_f32 v163, v218, v220
	v_add_f32_e32 v233, v218, v233
	v_add_f32_e32 v233, v220, v233
	v_exp_f32_e32 v222, v118
	v_exp_f32_e32 v224, v119
	v_mfma_f32_32x32x16_bf16 v[66:81], v[164:167], v[142:145], v[66:81]
	v_cvt_pk_bf16_f32 v164, v222, v224
	v_add_f32_e32 v233, v222, v233
	v_add_f32_e32 v233, v224, v233
	v_exp_f32_e32 v238, v120
	v_exp_f32_e32 v240, v121
	s_waitcnt lgkmcnt(1)
	v_mfma_f32_32x32x16_bf16 v[82:97], v[168:171], v[146:149], v[82:97]
	ds_read_b128 v[118:121], v0 offset:57344
	v_cvt_pk_bf16_f32 v165, v238, v240
	v_add_f32_e32 v233, v238, v233
	v_add_f32_e32 v233, v240, v233
	v_exp_f32_e32 v242, v122
	v_exp_f32_e32 v244, v123
	v_mfma_f32_32x32x16_bf16 v[66:81], v[168:171], v[150:153], v[66:81]
	ds_read_b128 v[234:237], v0 offset:57856
	v_cvt_pk_bf16_f32 v166, v242, v244
	v_add_f32_e32 v233, v242, v233
	v_add_f32_e32 v233, v244, v233
	v_exp_f32_e32 v246, v124
	v_exp_f32_e32 v248, v125
	s_waitcnt lgkmcnt(2)
	v_mfma_f32_32x32x16_bf16 v[82:97], v[114:117], v[154:157], v[82:97]
	v_cvt_pk_bf16_f32 v167, v246, v248
	v_add_f32_e32 v233, v246, v233
	v_add_f32_e32 v233, v248, v233
	v_exp_f32_e32 v126, v126
	v_exp_f32_e32 v212, v127
	v_mfma_f32_32x32x16_bf16 v[66:81], v[114:117], v[158:161], v[66:81]
	v_cvt_pk_bf16_f32 v168, v126, v212
	v_add_f32_e32 v233, v126, v233
	v_add_f32_e32 v233, v212, v233
	v_exp_f32_e32 v128, v128
	v_exp_f32_e32 v210, v129
	s_waitcnt lgkmcnt(1)
	v_mfma_f32_32x32x16_bf16 v[2:17], v[118:121], v[182:185], v[2:17]
	ds_read_b128 v[114:117], v0 offset:59392
	v_exp_f32_e32 v173, v98
	v_cvt_pk_bf16_f32 v169, v128, v210
	v_add_f32_e32 v233, v128, v233
	v_add_f32_e32 v233, v210, v233
	v_exp_f32_e32 v217, v99
	s_waitcnt lgkmcnt(1)
	v_mfma_f32_32x32x16_bf16 v[18:33], v[234:237], v[182:185], v[18:33]
	ds_read_b128 v[122:125], v0 offset:59904
	v_cvt_pk_bf16_f32 v174, v173, v217
	v_add_f32_e32 v227, v173, v227
	v_add_f32_e32 v227, v217, v227
	v_exp_f32_e32 v219, v100
	v_exp_f32_e32 v221, v101
	v_mfma_f32_32x32x16_bf16 v[34:49], v[118:121], v[190:193], v[34:49]
	v_cvt_pk_bf16_f32 v175, v219, v221
	v_add_f32_e32 v227, v219, v227
	v_add_f32_e32 v227, v221, v227
	v_exp_f32_e32 v223, v102
	v_exp_f32_e32 v225, v103
	v_mfma_f32_32x32x16_bf16 v[50:65], v[234:237], v[190:193], v[50:65]
	v_cvt_pk_bf16_f32 v176, v223, v225
	v_add_f32_e32 v227, v223, v227
	v_add_f32_e32 v227, v225, v227
	v_exp_f32_e32 v239, v104
	v_exp_f32_e32 v241, v105
	s_waitcnt lgkmcnt(1)
	v_mfma_f32_32x32x16_bf16 v[2:17], v[114:117], v[178:181], v[2:17]
	ds_read_b128 v[98:101], v215 offset:512
	v_cvt_pk_bf16_f32 v177, v239, v241
	v_add_f32_e32 v227, v239, v227
	v_add_f32_e32 v227, v241, v227
	v_exp_f32_e32 v243, v106
	v_exp_f32_e32 v245, v107
	s_waitcnt lgkmcnt(1)
	v_mfma_f32_32x32x16_bf16 v[18:33], v[122:125], v[178:181], v[18:33]
	v_cvt_pk_bf16_f32 v170, v243, v245
	v_add_f32_e32 v227, v243, v227
	v_add_f32_e32 v227, v245, v227
	v_exp_f32_e32 v247, v108
	v_exp_f32_e32 v249, v109
	v_mfma_f32_32x32x16_bf16 v[34:49], v[114:117], v[186:189], v[34:49]
	ds_read_b128 v[178:181], v215 offset:2560
	v_cvt_pk_bf16_f32 v171, v247, v249
	v_add_f32_e32 v227, v247, v227
	v_add_f32_e32 v227, v249, v227
	v_exp_f32_e32 v127, v110
	v_exp_f32_e32 v213, v111
	v_mfma_f32_32x32x16_bf16 v[50:65], v[122:125], v[186:189], v[50:65]
	v_exp_f32_e32 v129, v112
	v_exp_f32_e32 v211, v113
	v_cvt_pk_bf16_f32 v172, v127, v213
	v_add_f32_e32 v227, v127, v227
	v_add_f32_e32 v227, v213, v227
	v_cvt_pk_bf16_f32 v173, v129, v211
	v_add_f32_e32 v227, v129, v227
	v_add_f32_e32 v227, v211, v227
	s_waitcnt vmcnt(0)
	s_add_i32 s21, s21, 1
	s_mov_b32 s22, 3
	s_cmpk_eq_i32 s21, 0x104
	s_waitcnt vmcnt(0) lgkmcnt(0)
	s_barrier
	s_cbranch_scc0 .LBB0_967
	v_add_u32_e32 v232, 0xc000, v0
	v_mov_b32_e32 v186, v233
	v_mov_b32_e32 v187, v227
	v_mov_b32_e32 v227, 0x7c
	ds_read_b128 v[66:69], v232 offset:12288
	ds_read_b128 v[70:73], v232 offset:12800
	v_mov_b32_e32 v0, v230
	s_waitcnt lgkmcnt(1)
	v_mfma_f32_32x32x16_bf16 v[2:17], v[66:69], v[162:165], v[2:17]
	s_waitcnt lgkmcnt(0)
	v_mfma_f32_32x32x16_bf16 v[18:33], v[70:73], v[162:165], v[18:33]
	v_mfma_f32_32x32x16_bf16 v[34:49], v[66:69], v[174:177], v[34:49]
	v_mfma_f32_32x32x16_bf16 v[50:65], v[70:73], v[174:177], v[50:65]
	ds_read_b128 v[66:69], v232 offset:14336
	ds_read_b128 v[70:73], v232 offset:14848
	s_nop 0
	v_readfirstlane_b32 s16, v0
	s_ashr_i32 s16, s16, 1
	s_andn2_b32 s16, s16, 31
	s_cmpk_lt_i32 s16, 0x100
	s_waitcnt lgkmcnt(1)
	v_mfma_f32_32x32x16_bf16 v[2:17], v[66:69], v[166:169], v[2:17]
	s_waitcnt lgkmcnt(0)
	v_mfma_f32_32x32x16_bf16 v[18:33], v[70:73], v[166:169], v[18:33]
	v_mfma_f32_32x32x16_bf16 v[34:49], v[66:69], v[170:173], v[34:49]
	v_mbcnt_lo_u32_b32 v66, -1, 0
	v_mbcnt_hi_u32_b32 v66, -1, v66
	v_mbcnt_lo_u32_b32 v67, -1, 0
	v_mbcnt_hi_u32_b32 v67, -1, v67
	s_nop 0
	v_lshlrev_b32_e32 v66, 2, v66
	v_lshlrev_b32_e32 v67, 2, v67
	v_xor_b32_e32 v66, 0x80, v66
	v_xor_b32_e32 v67, 0x80, v67
	v_mfma_f32_32x32x16_bf16 v[50:65], v[70:73], v[170:173], v[50:65]
	ds_bpermute_b32 v66, v66, v186
	ds_bpermute_b32 v67, v67, v187
	s_cbranch_scc0 .LBB0_965
	s_lshl_b64 s[6:7], s[6:7], 11
	s_waitcnt lgkmcnt(1)
	v_add_f32_e32 v66, v186, v66
	s_add_u32 s6, s2, s6
	v_rcp_f32_e32 v66, v66
	s_addc_u32 s7, s3, s7
	s_lshl_b32 s15, s15, 1
	v_and_or_b32 v68, v0, 31, s16
	s_add_u32 s6, s6, s15
	v_ashrrev_i32_e32 v69, 31, v68
	s_addc_u32 s7, s7, 0
	s_waitcnt lgkmcnt(0)
	v_add_f32_e32 v67, v187, v67
	v_lshlrev_b64 v[68:69], 11, v[68:69]
	v_lshrrev_b32_e32 v0, 2, v0
	v_rcp_f32_e32 v70, v67
	v_lshl_add_u64 v[68:69], s[6:7], 0, v[68:69]
	v_pk_mul_f32 v[2:3], v[2:3], v[66:67] op_sel_hi:[1,0]
	v_pk_mul_f32 v[4:5], v[4:5], v[66:67] op_sel_hi:[1,0]
	v_and_b32_e32 v0, 8, v0
	v_pk_mul_f32 v[18:19], v[18:19], v[66:67] op_sel_hi:[1,0]
	v_pk_mul_f32 v[20:21], v[20:21], v[66:67] op_sel_hi:[1,0]
	v_pk_mul_f32 v[22:23], v[22:23], v[66:67] op_sel_hi:[1,0]
	v_pk_mul_f32 v[24:25], v[24:25], v[66:67] op_sel_hi:[1,0]
	v_pk_mul_f32 v[26:27], v[26:27], v[66:67] op_sel_hi:[1,0]
	v_pk_mul_f32 v[28:29], v[28:29], v[66:67] op_sel_hi:[1,0]
	v_pk_mul_f32 v[30:31], v[30:31], v[66:67] op_sel_hi:[1,0]
	v_pk_mul_f32 v[32:33], v[32:33], v[66:67] op_sel_hi:[1,0]
	v_pk_mul_f32 v[6:7], v[6:7], v[66:67] op_sel_hi:[1,0]
	v_pk_mul_f32 v[8:9], v[8:9], v[66:67] op_sel_hi:[1,0]
	v_pk_mul_f32 v[10:11], v[10:11], v[66:67] op_sel_hi:[1,0]
	v_pk_mul_f32 v[12:13], v[12:13], v[66:67] op_sel_hi:[1,0]
	v_pk_mul_f32 v[14:15], v[14:15], v[66:67] op_sel_hi:[1,0]
	v_pk_mul_f32 v[16:17], v[16:17], v[66:67] op_sel_hi:[1,0]
	v_lshl_add_u64 v[66:67], v[68:69], 0, v[0:1]
	v_cvt_pk_bf16_f32 v2, v2, v3
	v_cvt_pk_bf16_f32 v3, v4, v5
	v_cvt_pk_bf16_f32 v4, v18, v19
	v_cvt_pk_bf16_f32 v5, v20, v21
	global_store_dwordx2 v[66:67], v[2:3], off offset:1536
	global_store_dwordx2 v[66:67], v[4:5], off offset:1600
	v_cvt_pk_bf16_f32 v2, v6, v7
	v_cvt_pk_bf16_f32 v3, v8, v9
	v_cvt_pk_bf16_f32 v4, v22, v23
	v_cvt_pk_bf16_f32 v5, v24, v25
	global_store_dwordx2 v[66:67], v[2:3], off offset:1552
	global_store_dwordx2 v[66:67], v[4:5], off offset:1616
	v_cvt_pk_bf16_f32 v2, v10, v11
	v_cvt_pk_bf16_f32 v3, v12, v13
	v_pk_mul_f32 v[34:35], v[34:35], v[70:71] op_sel_hi:[1,0]
	v_pk_mul_f32 v[36:37], v[36:37], v[70:71] op_sel_hi:[1,0]
	v_cvt_pk_bf16_f32 v4, v26, v27
	v_cvt_pk_bf16_f32 v5, v28, v29
	global_store_dwordx2 v[66:67], v[2:3], off offset:1568
	global_store_dwordx2 v[66:67], v[4:5], off offset:1632
	v_cvt_pk_bf16_f32 v2, v14, v15
	v_cvt_pk_bf16_f32 v3, v16, v17
	v_pk_mul_f32 v[50:51], v[50:51], v[70:71] op_sel_hi:[1,0]
	v_pk_mul_f32 v[52:53], v[52:53], v[70:71] op_sel_hi:[1,0]
	v_pk_mul_f32 v[38:39], v[38:39], v[70:71] op_sel_hi:[1,0]
	v_pk_mul_f32 v[40:41], v[40:41], v[70:71] op_sel_hi:[1,0]
	v_cvt_pk_bf16_f32 v4, v30, v31
	v_cvt_pk_bf16_f32 v5, v32, v33
	global_store_dwordx2 v[66:67], v[2:3], off offset:1584
	global_store_dwordx2 v[66:67], v[4:5], off offset:1648
	v_cvt_pk_bf16_f32 v2, v34, v35
	v_cvt_pk_bf16_f32 v3, v36, v37
	v_pk_mul_f32 v[54:55], v[54:55], v[70:71] op_sel_hi:[1,0]
	v_pk_mul_f32 v[56:57], v[56:57], v[70:71] op_sel_hi:[1,0]
	v_pk_mul_f32 v[42:43], v[42:43], v[70:71] op_sel_hi:[1,0]
	v_pk_mul_f32 v[44:45], v[44:45], v[70:71] op_sel_hi:[1,0]
	v_cvt_pk_bf16_f32 v4, v50, v51
	v_cvt_pk_bf16_f32 v5, v52, v53
	global_store_dwordx2 v[66:67], v[2:3], off offset:1664
	global_store_dwordx2 v[66:67], v[4:5], off offset:1728
	v_cvt_pk_bf16_f32 v2, v38, v39
	v_cvt_pk_bf16_f32 v3, v40, v41
	v_pk_mul_f32 v[58:59], v[58:59], v[70:71] op_sel_hi:[1,0]
	v_pk_mul_f32 v[60:61], v[60:61], v[70:71] op_sel_hi:[1,0]
	v_pk_mul_f32 v[46:47], v[46:47], v[70:71] op_sel_hi:[1,0]
	v_pk_mul_f32 v[48:49], v[48:49], v[70:71] op_sel_hi:[1,0]
	v_cvt_pk_bf16_f32 v4, v54, v55
	v_cvt_pk_bf16_f32 v5, v56, v57
	global_store_dwordx2 v[66:67], v[2:3], off offset:1680
	global_store_dwordx2 v[66:67], v[4:5], off offset:1744
	v_cvt_pk_bf16_f32 v2, v42, v43
	v_cvt_pk_bf16_f32 v3, v44, v45
	v_pk_mul_f32 v[62:63], v[62:63], v[70:71] op_sel_hi:[1,0]
	v_pk_mul_f32 v[64:65], v[64:65], v[70:71] op_sel_hi:[1,0]
	v_cvt_pk_bf16_f32 v4, v58, v59
	v_cvt_pk_bf16_f32 v5, v60, v61
	global_store_dwordx2 v[66:67], v[2:3], off offset:1696
	global_store_dwordx2 v[66:67], v[4:5], off offset:1760
	v_cvt_pk_bf16_f32 v2, v46, v47
	v_cvt_pk_bf16_f32 v3, v48, v49
	v_cvt_pk_bf16_f32 v4, v62, v63
	v_cvt_pk_bf16_f32 v5, v64, v65
	global_store_dwordx2 v[66:67], v[2:3], off offset:1712
	global_store_dwordx2 v[66:67], v[4:5], off offset:1776
	s_branch .LBB0_965
